# GEMM K-loops: next phase's B-fragment LDS reads issued between the current phase's MFMAs (after last use of each register), all 4 loops + peeled copies
# speedup vs baseline: 1.0146x; 1.0138x over previous
.LBB0_191:
	s_ashr_i32 s61, s60, 31
	s_lshl_b64 s[62:63], s[60:61], 19
	s_add_u32 s62, s12, s62
	s_addc_u32 s63, s13, s63
	s_ashr_i32 s59, s58, 31
	s_lshl_b64 s[64:65], s[58:59], 19
	s_add_u32 s64, s14, s64
	s_addc_u32 s65, s15, s65
	s_andn2_b64 vcc, exec, s[30:31]
	s_cbranch_vccnz .LBB0_195
	v_cmp_lt_i64_e32 vcc, s[68:69], v[142:143]
	s_and_b64 s[68:69], vcc, exec
	s_cselect_b32 s9, s63, s11
	s_cselect_b32 s59, s62, s10
	s_cselect_b32 s61, s65, s67
	s_cselect_b32 s86, s64, s66
	s_add_u32 s10, s10, 0x40080
	s_addc_u32 s11, s11, 0
	s_add_u32 s87, s66, 0x100
	s_addc_u32 s88, s67, 0
	s_mov_b32 s66, 0
	s_waitcnt vmcnt(0)
	v_add_u32_e32 v154, s77, v157
	ds_read_b128 v[146:149], v154
	ds_read_b128 v[150:153], v154 offset:1024
	ds_read_b128 v[164:167], v154 offset:2048
	ds_read_b128 v[168:171], v154 offset:3072
	s_add_i32 s89, s66, 2
	s_add_u32 s67, s10, 0xfffc0080
	s_addc_u32 s68, s11, -1
	s_cmp_eq_u32 s75, s66
	s_cselect_b32 s66, s86, s87
	s_cselect_b32 s69, s9, s68
	s_cselect_b32 s68, s59, s67
	s_cselect_b32 s67, s61, s88
	v_lshl_add_u64 v[206:207], s[10:11], 0, v[138:139]
	s_add_i32 m0, s52, 0xc000
	ds_read_b128 v[172:175], v159
	ds_read_b128 v[176:179], v159 offset:1024
	ds_read_b128 v[180:183], v159 offset:2048
	ds_read_b128 v[184:187], v159 offset:3072
	ds_read_b128 v[188:191], v159 offset:4096
	ds_read_b128 v[192:195], v159 offset:5120
	ds_read_b128 v[198:201], v159 offset:6144
	ds_read_b128 v[202:205], v159 offset:7168
	global_load_lds_dwordx4 v[206:207], off
	v_lshl_add_u64 v[206:207], s[10:11], 0, v[140:141]
	s_add_i32 m0, s52, 0xe000
	s_nop 0
	global_load_lds_dwordx4 v[206:207], off
	s_waitcnt lgkmcnt(8)
	s_barrier
	s_waitcnt lgkmcnt(0)
	s_setprio 1
	s_waitcnt lgkmcnt(0)
	v_mfma_i32_16x16x64_i8 v[62:65], v[146:149], v[172:175], 0
	v_mfma_i32_16x16x64_i8 v[58:61], v[164:167], v[172:175], 0
	v_mfma_i32_16x16x64_i8 v[54:57], v[146:149], v[180:183], 0
	v_mfma_i32_16x16x64_i8 v[50:53], v[164:167], v[180:183], 0
	v_mfma_i32_16x16x64_i8 v[46:49], v[146:149], v[188:191], 0
	v_mfma_i32_16x16x64_i8 v[42:45], v[164:167], v[188:191], 0
	v_mfma_i32_16x16x64_i8 v[38:41], v[146:149], v[198:201], 0
	v_mfma_i32_16x16x64_i8 v[34:37], v[164:167], v[198:201], 0
	v_mfma_i32_16x16x64_i8 v[62:65], v[150:153], v[176:179], v[62:65]
	v_mfma_i32_16x16x64_i8 v[58:61], v[168:171], v[176:179], v[58:61]
	v_mfma_i32_16x16x64_i8 v[54:57], v[150:153], v[184:187], v[54:57]
	v_mfma_i32_16x16x64_i8 v[50:53], v[168:171], v[184:187], v[50:53]
	v_mfma_i32_16x16x64_i8 v[46:49], v[150:153], v[192:195], v[46:49]
	v_mfma_i32_16x16x64_i8 v[42:45], v[168:171], v[192:195], v[42:45]
	v_mfma_i32_16x16x64_i8 v[38:41], v[150:153], v[202:205], v[38:41]
	v_mfma_i32_16x16x64_i8 v[34:37], v[168:171], v[202:205], v[34:37]
	s_setprio 0
	s_barrier
	s_add_i32 s90, s77, s4
	v_add_u32_e32 v154, s78, v157
	v_lshl_add_u64 v[222:223], s[66:67], 0, v[134:135]
	s_mov_b32 m0, s90
	ds_read_b128 v[206:209], v154
	ds_read_b128 v[210:213], v154 offset:1024
	ds_read_b128 v[214:217], v154 offset:2048
	ds_read_b128 v[218:221], v154 offset:3072
	global_load_lds_dwordx4 v[222:223], off
	v_lshl_add_u64 v[224:225], s[66:67], 0, v[130:131]
	s_add_i32 m0, s90, 0x2000
	s_nop 0
	global_load_lds_dwordx4 v[224:225], off
	s_barrier
	s_waitcnt lgkmcnt(0)
	s_setprio 1
	s_waitcnt lgkmcnt(0)
	v_mfma_i32_16x16x64_i8 v[126:129], v[206:209], v[172:175], 0
	v_mfma_i32_16x16x64_i8 v[122:125], v[214:217], v[172:175], 0
	ds_read_b128 v[172:175], v159 offset:16384
	v_mfma_i32_16x16x64_i8 v[118:121], v[206:209], v[180:183], 0
	v_mfma_i32_16x16x64_i8 v[114:117], v[214:217], v[180:183], 0
	ds_read_b128 v[180:183], v159 offset:18432
	v_mfma_i32_16x16x64_i8 v[110:113], v[206:209], v[188:191], 0
	v_mfma_i32_16x16x64_i8 v[106:109], v[214:217], v[188:191], 0
	ds_read_b128 v[188:191], v159 offset:20480
	v_mfma_i32_16x16x64_i8 v[102:105], v[206:209], v[198:201], 0
	v_mfma_i32_16x16x64_i8 v[98:101], v[214:217], v[198:201], 0
	ds_read_b128 v[198:201], v159 offset:22528
	v_mfma_i32_16x16x64_i8 v[126:129], v[210:213], v[176:179], v[126:129]
	v_mfma_i32_16x16x64_i8 v[122:125], v[218:221], v[176:179], v[122:125]
	ds_read_b128 v[176:179], v159 offset:17408
	v_mfma_i32_16x16x64_i8 v[118:121], v[210:213], v[184:187], v[118:121]
	v_mfma_i32_16x16x64_i8 v[114:117], v[218:221], v[184:187], v[114:117]
	ds_read_b128 v[184:187], v159 offset:19456
	v_mfma_i32_16x16x64_i8 v[110:113], v[210:213], v[192:195], v[110:113]
	v_mfma_i32_16x16x64_i8 v[106:109], v[218:221], v[192:195], v[106:109]
	ds_read_b128 v[192:195], v159 offset:21504
	v_mfma_i32_16x16x64_i8 v[102:105], v[210:213], v[202:205], v[102:105]
	v_mfma_i32_16x16x64_i8 v[98:101], v[218:221], v[202:205], v[98:101]
	ds_read_b128 v[202:205], v159 offset:23552
	s_setprio 0
	s_mov_b32 m0, s52
	v_lshl_add_u64 v[226:227], s[68:69], 0, v[136:137]
	s_barrier
	global_load_lds_dwordx4 v[226:227], off
	v_lshl_add_u64 v[228:229], s[68:69], 0, v[132:133]
	s_mov_b32 m0, s53
	s_nop 0
	global_load_lds_dwordx4 v[228:229], off
	s_barrier
	s_waitcnt lgkmcnt(0)
	s_setprio 1
	s_waitcnt lgkmcnt(0)
	v_mfma_i32_16x16x64_i8 v[30:33], v[146:149], v[172:175], 0
	v_mfma_i32_16x16x64_i8 v[26:29], v[164:167], v[172:175], 0
	v_mfma_i32_16x16x64_i8 v[22:25], v[146:149], v[180:183], 0
	v_mfma_i32_16x16x64_i8 v[18:21], v[164:167], v[180:183], 0
	v_mfma_i32_16x16x64_i8 v[14:17], v[146:149], v[188:191], 0
	v_mfma_i32_16x16x64_i8 v[10:13], v[164:167], v[188:191], 0
	v_mfma_i32_16x16x64_i8 v[6:9], v[146:149], v[198:201], 0
	v_mfma_i32_16x16x64_i8 v[2:5], v[164:167], v[198:201], 0
	v_mfma_i32_16x16x64_i8 v[30:33], v[150:153], v[176:179], v[30:33]
	v_mfma_i32_16x16x64_i8 v[26:29], v[168:171], v[176:179], v[26:29]
	v_mfma_i32_16x16x64_i8 v[22:25], v[150:153], v[184:187], v[22:25]
	v_mfma_i32_16x16x64_i8 v[18:21], v[168:171], v[184:187], v[18:21]
	v_mfma_i32_16x16x64_i8 v[14:17], v[150:153], v[192:195], v[14:17]
	v_mfma_i32_16x16x64_i8 v[10:13], v[168:171], v[192:195], v[10:13]
	v_mfma_i32_16x16x64_i8 v[6:9], v[150:153], v[202:205], v[6:9]
	v_mfma_i32_16x16x64_i8 v[2:5], v[168:171], v[202:205], v[2:5]
	s_setprio 0
	s_barrier
	s_add_u32 s90, s66, 0x40000
	s_addc_u32 s91, s67, 0
	s_add_i32 s92, s78, s4
	v_lshl_add_u64 v[146:147], s[90:91], 0, v[134:135]
	s_mov_b32 m0, s92
	s_nop 0
	global_load_lds_dwordx4 v[146:147], off
	v_lshl_add_u64 v[146:147], s[90:91], 0, v[130:131]
	s_add_i32 m0, s92, 0x2000
	s_nop 0
	global_load_lds_dwordx4 v[146:147], off
	s_waitcnt vmcnt(6)
	s_barrier
	s_setprio 1
	v_mfma_i32_16x16x64_i8 v[94:97], v[206:209], v[172:175], 0
	v_mfma_i32_16x16x64_i8 v[90:93], v[214:217], v[172:175], 0
	ds_read_b128 v[172:175], v159 offset:32768
	v_mfma_i32_16x16x64_i8 v[86:89], v[206:209], v[180:183], 0
	v_mfma_i32_16x16x64_i8 v[82:85], v[214:217], v[180:183], 0
	ds_read_b128 v[180:183], v159 offset:34816
	v_mfma_i32_16x16x64_i8 v[78:81], v[206:209], v[188:191], 0
	v_mfma_i32_16x16x64_i8 v[74:77], v[214:217], v[188:191], 0
	ds_read_b128 v[188:191], v159 offset:36864
	v_mfma_i32_16x16x64_i8 v[70:73], v[206:209], v[198:201], 0
	v_mfma_i32_16x16x64_i8 v[66:69], v[214:217], v[198:201], 0
	ds_read_b128 v[198:201], v159 offset:38912
	v_mfma_i32_16x16x64_i8 v[94:97], v[210:213], v[176:179], v[94:97]
	v_mfma_i32_16x16x64_i8 v[90:93], v[218:221], v[176:179], v[90:93]
	ds_read_b128 v[176:179], v159 offset:33792
	v_mfma_i32_16x16x64_i8 v[86:89], v[210:213], v[184:187], v[86:89]
	v_mfma_i32_16x16x64_i8 v[82:85], v[218:221], v[184:187], v[82:85]
	ds_read_b128 v[184:187], v159 offset:35840
	v_mfma_i32_16x16x64_i8 v[78:81], v[210:213], v[192:195], v[78:81]
	v_mfma_i32_16x16x64_i8 v[74:77], v[218:221], v[192:195], v[74:77]
	ds_read_b128 v[192:195], v159 offset:37888
	v_mfma_i32_16x16x64_i8 v[70:73], v[210:213], v[202:205], v[70:73]
	v_mfma_i32_16x16x64_i8 v[66:69], v[218:221], v[202:205], v[66:69]
	ds_read_b128 v[202:205], v159 offset:39936
	s_setprio 0
	s_add_i32 s90, 0, 0x18000
	v_add_u32_e32 v154, s90, v157
	s_barrier
	ds_read_b128 v[146:149], v154
	ds_read_b128 v[150:153], v154 offset:1024
	ds_read_b128 v[164:167], v154 offset:2048
	ds_read_b128 v[168:171], v154 offset:3072
	s_add_u32 s68, s68, 0x40000
	s_addc_u32 s69, s69, 0
	s_mov_b32 m0, s54
	v_lshl_add_u64 v[206:207], s[68:69], 0, v[136:137]
	global_load_lds_dwordx4 v[206:207], off
	v_lshl_add_u64 v[206:207], s[68:69], 0, v[132:133]
	s_mov_b32 m0, s55
	s_nop 0
	global_load_lds_dwordx4 v[206:207], off
	s_waitcnt lgkmcnt(8)
	s_barrier
	s_waitcnt lgkmcnt(0)
	s_setprio 1
	s_waitcnt lgkmcnt(0)
	v_mfma_i32_16x16x64_i8 v[62:65], v[146:149], v[172:175], v[62:65]
	v_mfma_i32_16x16x64_i8 v[58:61], v[164:167], v[172:175], v[58:61]
	v_mfma_i32_16x16x64_i8 v[54:57], v[146:149], v[180:183], v[54:57]
	v_mfma_i32_16x16x64_i8 v[50:53], v[164:167], v[180:183], v[50:53]
	v_mfma_i32_16x16x64_i8 v[46:49], v[146:149], v[188:191], v[46:49]
	v_mfma_i32_16x16x64_i8 v[42:45], v[164:167], v[188:191], v[42:45]
	v_mfma_i32_16x16x64_i8 v[38:41], v[146:149], v[198:201], v[38:41]
	v_mfma_i32_16x16x64_i8 v[34:37], v[164:167], v[198:201], v[34:37]
	v_mfma_i32_16x16x64_i8 v[62:65], v[150:153], v[176:179], v[62:65]
	v_mfma_i32_16x16x64_i8 v[58:61], v[168:171], v[176:179], v[58:61]
	v_mfma_i32_16x16x64_i8 v[54:57], v[150:153], v[184:187], v[54:57]
	v_mfma_i32_16x16x64_i8 v[50:53], v[168:171], v[184:187], v[50:53]
	v_mfma_i32_16x16x64_i8 v[46:49], v[150:153], v[192:195], v[46:49]
	v_mfma_i32_16x16x64_i8 v[42:45], v[168:171], v[192:195], v[42:45]
	v_mfma_i32_16x16x64_i8 v[38:41], v[150:153], v[202:205], v[38:41]
	v_mfma_i32_16x16x64_i8 v[34:37], v[168:171], v[202:205], v[34:37]
	s_setprio 0
	s_barrier
	s_add_i32 s68, 0, 0x1c000
	s_add_i32 s69, s90, s4
	v_add_u32_e32 v154, s68, v157
	v_lshl_add_u64 v[222:223], v[222:223], 0, s[28:29]
	s_mov_b32 m0, s69
	ds_read_b128 v[206:209], v154
	ds_read_b128 v[210:213], v154 offset:1024
	ds_read_b128 v[214:217], v154 offset:2048
	ds_read_b128 v[218:221], v154 offset:3072
	global_load_lds_dwordx4 v[222:223], off
	v_lshl_add_u64 v[222:223], v[224:225], 0, s[28:29]
	s_add_i32 m0, s69, 0x2000
	s_nop 0
	global_load_lds_dwordx4 v[222:223], off
	s_barrier
	s_waitcnt lgkmcnt(0)
	s_setprio 1
	s_waitcnt lgkmcnt(0)
	v_mfma_i32_16x16x64_i8 v[126:129], v[206:209], v[172:175], v[126:129]
	v_mfma_i32_16x16x64_i8 v[122:125], v[214:217], v[172:175], v[122:125]
	ds_read_b128 v[172:175], v159 offset:49152
	v_mfma_i32_16x16x64_i8 v[118:121], v[206:209], v[180:183], v[118:121]
	v_mfma_i32_16x16x64_i8 v[114:117], v[214:217], v[180:183], v[114:117]
	ds_read_b128 v[180:183], v159 offset:51200
	v_mfma_i32_16x16x64_i8 v[110:113], v[206:209], v[188:191], v[110:113]
	v_mfma_i32_16x16x64_i8 v[106:109], v[214:217], v[188:191], v[106:109]
	ds_read_b128 v[188:191], v159 offset:53248
	v_mfma_i32_16x16x64_i8 v[102:105], v[206:209], v[198:201], v[102:105]
	v_mfma_i32_16x16x64_i8 v[98:101], v[214:217], v[198:201], v[98:101]
	ds_read_b128 v[198:201], v159 offset:55296
	v_mfma_i32_16x16x64_i8 v[126:129], v[210:213], v[176:179], v[126:129]
	v_mfma_i32_16x16x64_i8 v[122:125], v[218:221], v[176:179], v[122:125]
	ds_read_b128 v[176:179], v159 offset:50176
	v_mfma_i32_16x16x64_i8 v[118:121], v[210:213], v[184:187], v[118:121]
	v_mfma_i32_16x16x64_i8 v[114:117], v[218:221], v[184:187], v[114:117]
	ds_read_b128 v[184:187], v159 offset:52224
	v_mfma_i32_16x16x64_i8 v[110:113], v[210:213], v[192:195], v[110:113]
	v_mfma_i32_16x16x64_i8 v[106:109], v[218:221], v[192:195], v[106:109]
	ds_read_b128 v[192:195], v159 offset:54272
	v_mfma_i32_16x16x64_i8 v[102:105], v[210:213], v[202:205], v[102:105]
	v_mfma_i32_16x16x64_i8 v[98:101], v[218:221], v[202:205], v[98:101]
	ds_read_b128 v[202:205], v159 offset:56320
	s_setprio 0
	s_mov_b32 m0, s73
	v_lshl_add_u64 v[222:223], v[226:227], 0, s[28:29]
	s_barrier
	global_load_lds_dwordx4 v[222:223], off
	v_lshl_add_u64 v[222:223], v[228:229], 0, s[28:29]
	s_mov_b32 m0, s74
	s_nop 0
	global_load_lds_dwordx4 v[222:223], off
	s_barrier
	s_waitcnt lgkmcnt(0)
	s_setprio 1
	s_waitcnt lgkmcnt(0)
	v_mfma_i32_16x16x64_i8 v[30:33], v[146:149], v[172:175], v[30:33]
	v_mfma_i32_16x16x64_i8 v[26:29], v[164:167], v[172:175], v[26:29]
	v_mfma_i32_16x16x64_i8 v[22:25], v[146:149], v[180:183], v[22:25]
	v_mfma_i32_16x16x64_i8 v[18:21], v[164:167], v[180:183], v[18:21]
	v_mfma_i32_16x16x64_i8 v[14:17], v[146:149], v[188:191], v[14:17]
	v_mfma_i32_16x16x64_i8 v[10:13], v[164:167], v[188:191], v[10:13]
	v_mfma_i32_16x16x64_i8 v[6:9], v[146:149], v[198:201], v[6:9]
	v_mfma_i32_16x16x64_i8 v[2:5], v[164:167], v[198:201], v[2:5]
	v_mfma_i32_16x16x64_i8 v[30:33], v[150:153], v[176:179], v[30:33]
	v_mfma_i32_16x16x64_i8 v[26:29], v[168:171], v[176:179], v[26:29]
	v_mfma_i32_16x16x64_i8 v[22:25], v[150:153], v[184:187], v[22:25]
	v_mfma_i32_16x16x64_i8 v[18:21], v[168:171], v[184:187], v[18:21]
	v_mfma_i32_16x16x64_i8 v[14:17], v[150:153], v[192:195], v[14:17]
	v_mfma_i32_16x16x64_i8 v[10:13], v[168:171], v[192:195], v[10:13]
	v_mfma_i32_16x16x64_i8 v[6:9], v[150:153], v[202:205], v[6:9]
	v_mfma_i32_16x16x64_i8 v[2:5], v[168:171], v[202:205], v[2:5]
	s_setprio 0
	s_barrier
	s_add_u32 s66, s66, 0x40080
	s_addc_u32 s67, s67, 0
	s_add_i32 s68, s68, s4
	v_lshl_add_u64 v[146:147], s[66:67], 0, v[134:135]
	s_mov_b32 m0, s68
	s_nop 0
	global_load_lds_dwordx4 v[146:147], off
	v_lshl_add_u64 v[146:147], s[66:67], 0, v[130:131]
	s_add_i32 m0, s68, 0x2000
	s_nop 0
	global_load_lds_dwordx4 v[146:147], off
	s_waitcnt vmcnt(6)
	s_barrier
	s_setprio 1
	v_mfma_i32_16x16x64_i8 v[94:97], v[206:209], v[172:175], v[94:97]
	v_mfma_i32_16x16x64_i8 v[90:93], v[214:217], v[172:175], v[90:93]
	v_mfma_i32_16x16x64_i8 v[86:89], v[206:209], v[180:183], v[86:89]
	v_mfma_i32_16x16x64_i8 v[82:85], v[214:217], v[180:183], v[82:85]
	v_mfma_i32_16x16x64_i8 v[78:81], v[206:209], v[188:191], v[78:81]
	v_mfma_i32_16x16x64_i8 v[74:77], v[214:217], v[188:191], v[74:77]
	v_mfma_i32_16x16x64_i8 v[70:73], v[206:209], v[198:201], v[70:73]
	v_mfma_i32_16x16x64_i8 v[66:69], v[214:217], v[198:201], v[66:69]
	v_mfma_i32_16x16x64_i8 v[94:97], v[210:213], v[176:179], v[94:97]
	v_mfma_i32_16x16x64_i8 v[90:93], v[218:221], v[176:179], v[90:93]
	v_mfma_i32_16x16x64_i8 v[86:89], v[210:213], v[184:187], v[86:89]
	v_mfma_i32_16x16x64_i8 v[82:85], v[218:221], v[184:187], v[82:85]
	v_mfma_i32_16x16x64_i8 v[78:81], v[210:213], v[192:195], v[78:81]
	v_mfma_i32_16x16x64_i8 v[74:77], v[218:221], v[192:195], v[74:77]
	v_mfma_i32_16x16x64_i8 v[70:73], v[210:213], v[202:205], v[70:73]
	v_mfma_i32_16x16x64_i8 v[66:69], v[218:221], v[202:205], v[66:69]
	s_setprio 0
	s_add_u32 s10, s10, 0x100
	s_addc_u32 s11, s11, 0
	s_add_u32 s87, s87, 0x100
	s_addc_u32 s88, s88, 0
	s_cmp_ge_i32 s89, s1
	s_mov_b32 s66, s89
	s_barrier
	s_cbranch_scc0 .LBB0_193
	s_branch .Lmy_pl0_exit
.LBB0_193:
	s_waitcnt vmcnt(0)
	v_add_u32_e32 v154, s77, v157
	ds_read_b128 v[146:149], v154
	ds_read_b128 v[150:153], v154 offset:1024
	ds_read_b128 v[164:167], v154 offset:2048
	ds_read_b128 v[168:171], v154 offset:3072
	s_add_i32 s89, s66, 2
	s_add_u32 s67, s10, 0xfffc0080
	s_addc_u32 s68, s11, -1
	s_cmp_eq_u32 s75, s66
	s_cselect_b32 s66, s86, s87
	s_cselect_b32 s69, s9, s68
	s_cselect_b32 s68, s59, s67
	s_cselect_b32 s67, s61, s88
	v_lshl_add_u64 v[206:207], s[10:11], 0, v[138:139]
	s_add_i32 m0, s52, 0xc000
	ds_read_b128 v[172:175], v159
	ds_read_b128 v[176:179], v159 offset:1024
	ds_read_b128 v[180:183], v159 offset:2048
	ds_read_b128 v[184:187], v159 offset:3072
	ds_read_b128 v[188:191], v159 offset:4096
	ds_read_b128 v[192:195], v159 offset:5120
	ds_read_b128 v[198:201], v159 offset:6144
	ds_read_b128 v[202:205], v159 offset:7168
	global_load_lds_dwordx4 v[206:207], off
	v_lshl_add_u64 v[206:207], s[10:11], 0, v[140:141]
	s_add_i32 m0, s52, 0xe000
	s_nop 0
	global_load_lds_dwordx4 v[206:207], off
	s_waitcnt lgkmcnt(8)
	s_barrier
	s_waitcnt lgkmcnt(0)
	s_setprio 1
	s_waitcnt lgkmcnt(0)
	v_mfma_i32_16x16x64_i8 v[62:65], v[146:149], v[172:175], v[62:65]
	v_mfma_i32_16x16x64_i8 v[58:61], v[164:167], v[172:175], v[58:61]
	v_mfma_i32_16x16x64_i8 v[54:57], v[146:149], v[180:183], v[54:57]
	v_mfma_i32_16x16x64_i8 v[50:53], v[164:167], v[180:183], v[50:53]
	v_mfma_i32_16x16x64_i8 v[46:49], v[146:149], v[188:191], v[46:49]
	v_mfma_i32_16x16x64_i8 v[42:45], v[164:167], v[188:191], v[42:45]
	v_mfma_i32_16x16x64_i8 v[38:41], v[146:149], v[198:201], v[38:41]
	v_mfma_i32_16x16x64_i8 v[34:37], v[164:167], v[198:201], v[34:37]
	v_mfma_i32_16x16x64_i8 v[62:65], v[150:153], v[176:179], v[62:65]
	v_mfma_i32_16x16x64_i8 v[58:61], v[168:171], v[176:179], v[58:61]
	v_mfma_i32_16x16x64_i8 v[54:57], v[150:153], v[184:187], v[54:57]
	v_mfma_i32_16x16x64_i8 v[50:53], v[168:171], v[184:187], v[50:53]
	v_mfma_i32_16x16x64_i8 v[46:49], v[150:153], v[192:195], v[46:49]
	v_mfma_i32_16x16x64_i8 v[42:45], v[168:171], v[192:195], v[42:45]
	v_mfma_i32_16x16x64_i8 v[38:41], v[150:153], v[202:205], v[38:41]
	v_mfma_i32_16x16x64_i8 v[34:37], v[168:171], v[202:205], v[34:37]
	s_setprio 0
	s_barrier
	s_add_i32 s90, s77, s4
	v_add_u32_e32 v154, s78, v157
	v_lshl_add_u64 v[222:223], s[66:67], 0, v[134:135]
	s_mov_b32 m0, s90
	ds_read_b128 v[206:209], v154
	ds_read_b128 v[210:213], v154 offset:1024
	ds_read_b128 v[214:217], v154 offset:2048
	ds_read_b128 v[218:221], v154 offset:3072
	global_load_lds_dwordx4 v[222:223], off
	v_lshl_add_u64 v[224:225], s[66:67], 0, v[130:131]
	s_add_i32 m0, s90, 0x2000
	s_nop 0
	global_load_lds_dwordx4 v[224:225], off
	s_barrier
	s_waitcnt lgkmcnt(0)
	s_setprio 1
	s_waitcnt lgkmcnt(0)
	v_mfma_i32_16x16x64_i8 v[126:129], v[206:209], v[172:175], v[126:129]
	v_mfma_i32_16x16x64_i8 v[122:125], v[214:217], v[172:175], v[122:125]
	ds_read_b128 v[172:175], v159 offset:16384
	v_mfma_i32_16x16x64_i8 v[118:121], v[206:209], v[180:183], v[118:121]
	v_mfma_i32_16x16x64_i8 v[114:117], v[214:217], v[180:183], v[114:117]
	ds_read_b128 v[180:183], v159 offset:18432
	v_mfma_i32_16x16x64_i8 v[110:113], v[206:209], v[188:191], v[110:113]
	v_mfma_i32_16x16x64_i8 v[106:109], v[214:217], v[188:191], v[106:109]
	ds_read_b128 v[188:191], v159 offset:20480
	v_mfma_i32_16x16x64_i8 v[102:105], v[206:209], v[198:201], v[102:105]
	v_mfma_i32_16x16x64_i8 v[98:101], v[214:217], v[198:201], v[98:101]
	ds_read_b128 v[198:201], v159 offset:22528
	v_mfma_i32_16x16x64_i8 v[126:129], v[210:213], v[176:179], v[126:129]
	v_mfma_i32_16x16x64_i8 v[122:125], v[218:221], v[176:179], v[122:125]
	ds_read_b128 v[176:179], v159 offset:17408
	v_mfma_i32_16x16x64_i8 v[118:121], v[210:213], v[184:187], v[118:121]
	v_mfma_i32_16x16x64_i8 v[114:117], v[218:221], v[184:187], v[114:117]
	ds_read_b128 v[184:187], v159 offset:19456
	v_mfma_i32_16x16x64_i8 v[110:113], v[210:213], v[192:195], v[110:113]
	v_mfma_i32_16x16x64_i8 v[106:109], v[218:221], v[192:195], v[106:109]
	ds_read_b128 v[192:195], v159 offset:21504
	v_mfma_i32_16x16x64_i8 v[102:105], v[210:213], v[202:205], v[102:105]
	v_mfma_i32_16x16x64_i8 v[98:101], v[218:221], v[202:205], v[98:101]
	ds_read_b128 v[202:205], v159 offset:23552
	s_setprio 0
	s_mov_b32 m0, s52
	v_lshl_add_u64 v[226:227], s[68:69], 0, v[136:137]
	s_barrier
	global_load_lds_dwordx4 v[226:227], off
	v_lshl_add_u64 v[228:229], s[68:69], 0, v[132:133]
	s_mov_b32 m0, s53
	s_nop 0
	global_load_lds_dwordx4 v[228:229], off
	s_barrier
	s_waitcnt lgkmcnt(0)
	s_setprio 1
	s_waitcnt lgkmcnt(0)
	v_mfma_i32_16x16x64_i8 v[30:33], v[146:149], v[172:175], v[30:33]
	v_mfma_i32_16x16x64_i8 v[26:29], v[164:167], v[172:175], v[26:29]
	v_mfma_i32_16x16x64_i8 v[22:25], v[146:149], v[180:183], v[22:25]
	v_mfma_i32_16x16x64_i8 v[18:21], v[164:167], v[180:183], v[18:21]
	v_mfma_i32_16x16x64_i8 v[14:17], v[146:149], v[188:191], v[14:17]
	v_mfma_i32_16x16x64_i8 v[10:13], v[164:167], v[188:191], v[10:13]
	v_mfma_i32_16x16x64_i8 v[6:9], v[146:149], v[198:201], v[6:9]
	v_mfma_i32_16x16x64_i8 v[2:5], v[164:167], v[198:201], v[2:5]
	v_mfma_i32_16x16x64_i8 v[30:33], v[150:153], v[176:179], v[30:33]
	v_mfma_i32_16x16x64_i8 v[26:29], v[168:171], v[176:179], v[26:29]
	v_mfma_i32_16x16x64_i8 v[22:25], v[150:153], v[184:187], v[22:25]
	v_mfma_i32_16x16x64_i8 v[18:21], v[168:171], v[184:187], v[18:21]
	v_mfma_i32_16x16x64_i8 v[14:17], v[150:153], v[192:195], v[14:17]
	v_mfma_i32_16x16x64_i8 v[10:13], v[168:171], v[192:195], v[10:13]
	v_mfma_i32_16x16x64_i8 v[6:9], v[150:153], v[202:205], v[6:9]
	v_mfma_i32_16x16x64_i8 v[2:5], v[168:171], v[202:205], v[2:5]
	s_setprio 0
	s_barrier
	s_add_u32 s90, s66, 0x40000
	s_addc_u32 s91, s67, 0
	s_add_i32 s92, s78, s4
	v_lshl_add_u64 v[146:147], s[90:91], 0, v[134:135]
	s_mov_b32 m0, s92
	s_nop 0
	global_load_lds_dwordx4 v[146:147], off
	v_lshl_add_u64 v[146:147], s[90:91], 0, v[130:131]
	s_add_i32 m0, s92, 0x2000
	s_nop 0
	global_load_lds_dwordx4 v[146:147], off
	s_waitcnt vmcnt(6)
	s_barrier
	s_setprio 1
	v_mfma_i32_16x16x64_i8 v[94:97], v[206:209], v[172:175], v[94:97]
	v_mfma_i32_16x16x64_i8 v[90:93], v[214:217], v[172:175], v[90:93]
	ds_read_b128 v[172:175], v159 offset:32768
	v_mfma_i32_16x16x64_i8 v[86:89], v[206:209], v[180:183], v[86:89]
	v_mfma_i32_16x16x64_i8 v[82:85], v[214:217], v[180:183], v[82:85]
	ds_read_b128 v[180:183], v159 offset:34816
	v_mfma_i32_16x16x64_i8 v[78:81], v[206:209], v[188:191], v[78:81]
	v_mfma_i32_16x16x64_i8 v[74:77], v[214:217], v[188:191], v[74:77]
	ds_read_b128 v[188:191], v159 offset:36864
	v_mfma_i32_16x16x64_i8 v[70:73], v[206:209], v[198:201], v[70:73]
	v_mfma_i32_16x16x64_i8 v[66:69], v[214:217], v[198:201], v[66:69]
	ds_read_b128 v[198:201], v159 offset:38912
	v_mfma_i32_16x16x64_i8 v[94:97], v[210:213], v[176:179], v[94:97]
	v_mfma_i32_16x16x64_i8 v[90:93], v[218:221], v[176:179], v[90:93]
	ds_read_b128 v[176:179], v159 offset:33792
	v_mfma_i32_16x16x64_i8 v[86:89], v[210:213], v[184:187], v[86:89]
	v_mfma_i32_16x16x64_i8 v[82:85], v[218:221], v[184:187], v[82:85]
	ds_read_b128 v[184:187], v159 offset:35840
	v_mfma_i32_16x16x64_i8 v[78:81], v[210:213], v[192:195], v[78:81]
	v_mfma_i32_16x16x64_i8 v[74:77], v[218:221], v[192:195], v[74:77]
	ds_read_b128 v[192:195], v159 offset:37888
	v_mfma_i32_16x16x64_i8 v[70:73], v[210:213], v[202:205], v[70:73]
	v_mfma_i32_16x16x64_i8 v[66:69], v[218:221], v[202:205], v[66:69]
	ds_read_b128 v[202:205], v159 offset:39936
	s_setprio 0
	s_add_i32 s90, 0, 0x18000
	v_add_u32_e32 v154, s90, v157
	s_barrier
	ds_read_b128 v[146:149], v154
	ds_read_b128 v[150:153], v154 offset:1024
	ds_read_b128 v[164:167], v154 offset:2048
	ds_read_b128 v[168:171], v154 offset:3072
	s_add_u32 s68, s68, 0x40000
	s_addc_u32 s69, s69, 0
	s_mov_b32 m0, s54
	v_lshl_add_u64 v[206:207], s[68:69], 0, v[136:137]
	global_load_lds_dwordx4 v[206:207], off
	v_lshl_add_u64 v[206:207], s[68:69], 0, v[132:133]
	s_mov_b32 m0, s55
	s_nop 0
	global_load_lds_dwordx4 v[206:207], off
	s_waitcnt lgkmcnt(8)
	s_barrier
	s_waitcnt lgkmcnt(0)
	s_setprio 1
	s_waitcnt lgkmcnt(0)
	v_mfma_i32_16x16x64_i8 v[62:65], v[146:149], v[172:175], v[62:65]
	v_mfma_i32_16x16x64_i8 v[58:61], v[164:167], v[172:175], v[58:61]
	v_mfma_i32_16x16x64_i8 v[54:57], v[146:149], v[180:183], v[54:57]
	v_mfma_i32_16x16x64_i8 v[50:53], v[164:167], v[180:183], v[50:53]
	v_mfma_i32_16x16x64_i8 v[46:49], v[146:149], v[188:191], v[46:49]
	v_mfma_i32_16x16x64_i8 v[42:45], v[164:167], v[188:191], v[42:45]
	v_mfma_i32_16x16x64_i8 v[38:41], v[146:149], v[198:201], v[38:41]
	v_mfma_i32_16x16x64_i8 v[34:37], v[164:167], v[198:201], v[34:37]
	v_mfma_i32_16x16x64_i8 v[62:65], v[150:153], v[176:179], v[62:65]
	v_mfma_i32_16x16x64_i8 v[58:61], v[168:171], v[176:179], v[58:61]
	v_mfma_i32_16x16x64_i8 v[54:57], v[150:153], v[184:187], v[54:57]
	v_mfma_i32_16x16x64_i8 v[50:53], v[168:171], v[184:187], v[50:53]
	v_mfma_i32_16x16x64_i8 v[46:49], v[150:153], v[192:195], v[46:49]
	v_mfma_i32_16x16x64_i8 v[42:45], v[168:171], v[192:195], v[42:45]
	v_mfma_i32_16x16x64_i8 v[38:41], v[150:153], v[202:205], v[38:41]
	v_mfma_i32_16x16x64_i8 v[34:37], v[168:171], v[202:205], v[34:37]
	s_setprio 0
	s_barrier
	s_add_i32 s68, 0, 0x1c000
	s_add_i32 s69, s90, s4
	v_add_u32_e32 v154, s68, v157
	v_lshl_add_u64 v[222:223], v[222:223], 0, s[28:29]
	s_mov_b32 m0, s69
	ds_read_b128 v[206:209], v154
	ds_read_b128 v[210:213], v154 offset:1024
	ds_read_b128 v[214:217], v154 offset:2048
	ds_read_b128 v[218:221], v154 offset:3072
	global_load_lds_dwordx4 v[222:223], off
	v_lshl_add_u64 v[222:223], v[224:225], 0, s[28:29]
	s_add_i32 m0, s69, 0x2000
	s_nop 0
	global_load_lds_dwordx4 v[222:223], off
	s_barrier
	s_waitcnt lgkmcnt(0)
	s_setprio 1
	s_waitcnt lgkmcnt(0)
	v_mfma_i32_16x16x64_i8 v[126:129], v[206:209], v[172:175], v[126:129]
	v_mfma_i32_16x16x64_i8 v[122:125], v[214:217], v[172:175], v[122:125]
	ds_read_b128 v[172:175], v159 offset:49152
	v_mfma_i32_16x16x64_i8 v[118:121], v[206:209], v[180:183], v[118:121]
	v_mfma_i32_16x16x64_i8 v[114:117], v[214:217], v[180:183], v[114:117]
	ds_read_b128 v[180:183], v159 offset:51200
	v_mfma_i32_16x16x64_i8 v[110:113], v[206:209], v[188:191], v[110:113]
	v_mfma_i32_16x16x64_i8 v[106:109], v[214:217], v[188:191], v[106:109]
	ds_read_b128 v[188:191], v159 offset:53248
	v_mfma_i32_16x16x64_i8 v[102:105], v[206:209], v[198:201], v[102:105]
	v_mfma_i32_16x16x64_i8 v[98:101], v[214:217], v[198:201], v[98:101]
	ds_read_b128 v[198:201], v159 offset:55296
	v_mfma_i32_16x16x64_i8 v[126:129], v[210:213], v[176:179], v[126:129]
	v_mfma_i32_16x16x64_i8 v[122:125], v[218:221], v[176:179], v[122:125]
	ds_read_b128 v[176:179], v159 offset:50176
	v_mfma_i32_16x16x64_i8 v[118:121], v[210:213], v[184:187], v[118:121]
	v_mfma_i32_16x16x64_i8 v[114:117], v[218:221], v[184:187], v[114:117]
	ds_read_b128 v[184:187], v159 offset:52224
	v_mfma_i32_16x16x64_i8 v[110:113], v[210:213], v[192:195], v[110:113]
	v_mfma_i32_16x16x64_i8 v[106:109], v[218:221], v[192:195], v[106:109]
	ds_read_b128 v[192:195], v159 offset:54272
	v_mfma_i32_16x16x64_i8 v[102:105], v[210:213], v[202:205], v[102:105]
	v_mfma_i32_16x16x64_i8 v[98:101], v[218:221], v[202:205], v[98:101]
	ds_read_b128 v[202:205], v159 offset:56320
	s_setprio 0
	s_mov_b32 m0, s73
	v_lshl_add_u64 v[222:223], v[226:227], 0, s[28:29]
	s_barrier
	global_load_lds_dwordx4 v[222:223], off
	v_lshl_add_u64 v[222:223], v[228:229], 0, s[28:29]
	s_mov_b32 m0, s74
	s_nop 0
	global_load_lds_dwordx4 v[222:223], off
	s_barrier
	s_waitcnt lgkmcnt(0)
	s_setprio 1
	s_waitcnt lgkmcnt(0)
	v_mfma_i32_16x16x64_i8 v[30:33], v[146:149], v[172:175], v[30:33]
	v_mfma_i32_16x16x64_i8 v[26:29], v[164:167], v[172:175], v[26:29]
	v_mfma_i32_16x16x64_i8 v[22:25], v[146:149], v[180:183], v[22:25]
	v_mfma_i32_16x16x64_i8 v[18:21], v[164:167], v[180:183], v[18:21]
	v_mfma_i32_16x16x64_i8 v[14:17], v[146:149], v[188:191], v[14:17]
	v_mfma_i32_16x16x64_i8 v[10:13], v[164:167], v[188:191], v[10:13]
	v_mfma_i32_16x16x64_i8 v[6:9], v[146:149], v[198:201], v[6:9]
	v_mfma_i32_16x16x64_i8 v[2:5], v[164:167], v[198:201], v[2:5]
	v_mfma_i32_16x16x64_i8 v[30:33], v[150:153], v[176:179], v[30:33]
	v_mfma_i32_16x16x64_i8 v[26:29], v[168:171], v[176:179], v[26:29]
	v_mfma_i32_16x16x64_i8 v[22:25], v[150:153], v[184:187], v[22:25]
	v_mfma_i32_16x16x64_i8 v[18:21], v[168:171], v[184:187], v[18:21]
	v_mfma_i32_16x16x64_i8 v[14:17], v[150:153], v[192:195], v[14:17]
	v_mfma_i32_16x16x64_i8 v[10:13], v[168:171], v[192:195], v[10:13]
	v_mfma_i32_16x16x64_i8 v[6:9], v[150:153], v[202:205], v[6:9]
	v_mfma_i32_16x16x64_i8 v[2:5], v[168:171], v[202:205], v[2:5]
	s_setprio 0
	s_barrier
	s_add_u32 s66, s66, 0x40080
	s_addc_u32 s67, s67, 0
	s_add_i32 s68, s68, s4
	v_lshl_add_u64 v[146:147], s[66:67], 0, v[134:135]
	s_mov_b32 m0, s68
	s_nop 0
	global_load_lds_dwordx4 v[146:147], off
	v_lshl_add_u64 v[146:147], s[66:67], 0, v[130:131]
	s_add_i32 m0, s68, 0x2000
	s_nop 0
	global_load_lds_dwordx4 v[146:147], off
	s_waitcnt vmcnt(6)
	s_barrier
	s_setprio 1
	v_mfma_i32_16x16x64_i8 v[94:97], v[206:209], v[172:175], v[94:97]
	v_mfma_i32_16x16x64_i8 v[90:93], v[214:217], v[172:175], v[90:93]
	v_mfma_i32_16x16x64_i8 v[86:89], v[206:209], v[180:183], v[86:89]
	v_mfma_i32_16x16x64_i8 v[82:85], v[214:217], v[180:183], v[82:85]
	v_mfma_i32_16x16x64_i8 v[78:81], v[206:209], v[188:191], v[78:81]
	v_mfma_i32_16x16x64_i8 v[74:77], v[214:217], v[188:191], v[74:77]
	v_mfma_i32_16x16x64_i8 v[70:73], v[206:209], v[198:201], v[70:73]
	v_mfma_i32_16x16x64_i8 v[66:69], v[214:217], v[198:201], v[66:69]
	v_mfma_i32_16x16x64_i8 v[94:97], v[210:213], v[176:179], v[94:97]
	v_mfma_i32_16x16x64_i8 v[90:93], v[218:221], v[176:179], v[90:93]
	v_mfma_i32_16x16x64_i8 v[86:89], v[210:213], v[184:187], v[86:89]
	v_mfma_i32_16x16x64_i8 v[82:85], v[218:221], v[184:187], v[82:85]
	v_mfma_i32_16x16x64_i8 v[78:81], v[210:213], v[192:195], v[78:81]
	v_mfma_i32_16x16x64_i8 v[74:77], v[218:221], v[192:195], v[74:77]
	v_mfma_i32_16x16x64_i8 v[70:73], v[210:213], v[202:205], v[70:73]
	v_mfma_i32_16x16x64_i8 v[66:69], v[218:221], v[202:205], v[66:69]
	s_setprio 0
	s_add_u32 s10, s10, 0x100
	s_addc_u32 s11, s11, 0
	s_add_u32 s87, s87, 0x100
	s_addc_u32 s88, s88, 0
	s_cmp_ge_i32 s89, s1
	s_mov_b32 s66, s89
	s_barrier
	s_cbranch_scc0 .LBB0_193

.LBB0_962:
	s_ashr_i32 s27, s26, 31
	s_lshl_b64 s[28:29], s[26:27], 20
	s_add_u32 s28, s10, s28
	s_addc_u32 s29, s11, s29
	s_ashr_i32 s25, s24, 31
	s_lshl_b64 s[30:31], s[24:25], 20
	s_add_u32 s30, s14, s30
	v_cmp_lt_i64_e64 s[8:9], s[8:9], v[158:159]
	s_addc_u32 s31, s15, s31
	s_andn2_b64 vcc, exec, s[20:21]
	s_cbranch_vccnz .LBB0_954
	s_and_b64 s[8:9], s[8:9], exec
	s_cselect_b32 s25, s29, s39
	s_cselect_b32 s27, s28, s38
	s_cselect_b32 s51, s31, s37
	s_cselect_b32 s52, s30, s36
	s_add_u32 s8, s38, 0x80080
	s_addc_u32 s9, s39, 0
	s_add_u32 s53, s36, 0x100
	v_mov_b32_e32 v2, 0
	s_addc_u32 s54, s37, 0
	s_mov_b32 s36, 0
	ds_read_b128 v[130:133], v172
	ds_read_b128 v[134:137], v172 offset:1024
	ds_read_b128 v[138:141], v172 offset:2048
	ds_read_b128 v[142:145], v172 offset:3072
	s_add_i32 s55, s36, 2
	s_add_u32 s37, s8, 0xfff80080
	s_addc_u32 s38, s9, -1
	s_cmp_eq_u32 s46, s36
	s_cselect_b32 s36, s52, s53
	s_cselect_b32 s39, s25, s38
	s_cselect_b32 s38, s27, s37
	s_cselect_b32 s37, s51, s54
	v_lshl_add_u64 v[200:201], s[8:9], 0, v[154:155]
	s_add_i32 m0, s23, 0xc000
	ds_read_b128 v[162:165], v173
	ds_read_b128 v[166:169], v173 offset:1024
	ds_read_b128 v[176:179], v173 offset:2048
	ds_read_b128 v[180:183], v173 offset:3072
	ds_read_b128 v[184:187], v173 offset:4096
	ds_read_b128 v[188:191], v173 offset:5120
	ds_read_b128 v[192:195], v173 offset:6144
	ds_read_b128 v[196:199], v173 offset:7168
	global_load_lds_dwordx4 v[200:201], off
	v_lshl_add_u64 v[200:201], s[8:9], 0, v[156:157]
	s_add_i32 m0, s23, 0xe000
	s_nop 0
	global_load_lds_dwordx4 v[200:201], off
	s_waitcnt lgkmcnt(8)
	s_barrier
	s_waitcnt lgkmcnt(0)
	s_setprio 1
	s_waitcnt lgkmcnt(0)
	v_mfma_f32_16x16x32_bf16 v[126:129], v[130:133], v[162:165], 0
	ds_read_b128 v[200:203], v174
	ds_read_b128 v[204:207], v174 offset:1024
	ds_read_b128 v[208:211], v174 offset:2048
	ds_read_b128 v[214:217], v174 offset:3072
	v_mfma_f32_16x16x32_bf16 v[122:125], v[138:141], v[162:165], 0
	v_mfma_f32_16x16x32_bf16 v[110:113], v[130:133], v[176:179], 0
	v_mfma_f32_16x16x32_bf16 v[106:109], v[138:141], v[176:179], 0
	v_mfma_f32_16x16x32_bf16 v[94:97], v[130:133], v[184:187], 0
	v_mfma_f32_16x16x32_bf16 v[90:93], v[138:141], v[184:187], 0
	v_mfma_f32_16x16x32_bf16 v[78:81], v[130:133], v[192:195], 0
	v_mfma_f32_16x16x32_bf16 v[74:77], v[138:141], v[192:195], 0
	v_mfma_f32_16x16x32_bf16 v[126:129], v[134:137], v[166:169], v[126:129]
	v_mfma_f32_16x16x32_bf16 v[122:125], v[142:145], v[166:169], v[122:125]
	v_mfma_f32_16x16x32_bf16 v[110:113], v[134:137], v[180:183], v[110:113]
	v_mfma_f32_16x16x32_bf16 v[106:109], v[142:145], v[180:183], v[106:109]
	v_mfma_f32_16x16x32_bf16 v[94:97], v[134:137], v[188:191], v[94:97]
	v_mfma_f32_16x16x32_bf16 v[90:93], v[142:145], v[188:191], v[90:93]
	v_mfma_f32_16x16x32_bf16 v[78:81], v[134:137], v[196:199], v[78:81]
	v_mfma_f32_16x16x32_bf16 v[74:77], v[142:145], v[196:199], v[74:77]
	s_setprio 0
	s_barrier
	s_add_i32 s56, s48, s5
	v_lshl_add_u64 v[218:219], s[36:37], 0, v[148:149]
	s_mov_b32 m0, s56
	global_load_lds_dwordx4 v[218:219], off
	v_lshl_add_u64 v[220:221], s[36:37], 0, v[152:153]
	s_add_i32 m0, s56, 0x2000
	s_nop 0
	global_load_lds_dwordx4 v[220:221], off
	s_barrier
	s_waitcnt lgkmcnt(0)
	s_setprio 1
	s_waitcnt lgkmcnt(0)
	v_mfma_f32_16x16x32_bf16 v[118:121], v[200:203], v[162:165], 0
	v_mfma_f32_16x16x32_bf16 v[114:117], v[208:211], v[162:165], 0
	ds_read_b128 v[162:165], v173 offset:16384
	v_mfma_f32_16x16x32_bf16 v[102:105], v[200:203], v[176:179], 0
	v_mfma_f32_16x16x32_bf16 v[98:101], v[208:211], v[176:179], 0
	ds_read_b128 v[176:179], v173 offset:18432
	v_mfma_f32_16x16x32_bf16 v[86:89], v[200:203], v[184:187], 0
	v_mfma_f32_16x16x32_bf16 v[82:85], v[208:211], v[184:187], 0
	ds_read_b128 v[184:187], v173 offset:20480
	v_mfma_f32_16x16x32_bf16 v[70:73], v[200:203], v[192:195], 0
	v_mfma_f32_16x16x32_bf16 v[66:69], v[208:211], v[192:195], 0
	ds_read_b128 v[192:195], v173 offset:22528
	v_mfma_f32_16x16x32_bf16 v[118:121], v[204:207], v[166:169], v[118:121]
	v_mfma_f32_16x16x32_bf16 v[114:117], v[214:217], v[166:169], v[114:117]
	ds_read_b128 v[166:169], v173 offset:17408
	v_mfma_f32_16x16x32_bf16 v[102:105], v[204:207], v[180:183], v[102:105]
	v_mfma_f32_16x16x32_bf16 v[98:101], v[214:217], v[180:183], v[98:101]
	ds_read_b128 v[180:183], v173 offset:19456
	v_mfma_f32_16x16x32_bf16 v[86:89], v[204:207], v[188:191], v[86:89]
	v_mfma_f32_16x16x32_bf16 v[82:85], v[214:217], v[188:191], v[82:85]
	ds_read_b128 v[188:191], v173 offset:21504
	v_mfma_f32_16x16x32_bf16 v[70:73], v[204:207], v[196:199], v[70:73]
	v_mfma_f32_16x16x32_bf16 v[66:69], v[214:217], v[196:199], v[66:69]
	ds_read_b128 v[196:199], v173 offset:23552
	s_setprio 0
	s_mov_b32 m0, s23
	v_lshl_add_u64 v[222:223], s[38:39], 0, v[146:147]
	s_barrier
	global_load_lds_dwordx4 v[222:223], off
	v_lshl_add_u64 v[224:225], s[38:39], 0, v[150:151]
	s_mov_b32 m0, s33
	s_nop 0
	global_load_lds_dwordx4 v[224:225], off
	s_barrier
	s_waitcnt lgkmcnt(0)
	s_setprio 1
	s_waitcnt lgkmcnt(0)
	v_mfma_f32_16x16x32_bf16 v[62:65], v[130:133], v[162:165], 0
	v_mfma_f32_16x16x32_bf16 v[58:61], v[138:141], v[162:165], 0
	v_mfma_f32_16x16x32_bf16 v[46:49], v[130:133], v[176:179], 0
	v_mfma_f32_16x16x32_bf16 v[42:45], v[138:141], v[176:179], 0
	v_mfma_f32_16x16x32_bf16 v[30:33], v[130:133], v[184:187], 0
	v_mfma_f32_16x16x32_bf16 v[26:29], v[138:141], v[184:187], 0
	v_mfma_f32_16x16x32_bf16 v[14:17], v[130:133], v[192:195], 0
	v_mfma_f32_16x16x32_bf16 v[10:13], v[138:141], v[192:195], 0
	v_mfma_f32_16x16x32_bf16 v[62:65], v[134:137], v[166:169], v[62:65]
	v_mfma_f32_16x16x32_bf16 v[58:61], v[142:145], v[166:169], v[58:61]
	v_mfma_f32_16x16x32_bf16 v[46:49], v[134:137], v[180:183], v[46:49]
	v_mfma_f32_16x16x32_bf16 v[42:45], v[142:145], v[180:183], v[42:45]
	v_mfma_f32_16x16x32_bf16 v[30:33], v[134:137], v[188:191], v[30:33]
	v_mfma_f32_16x16x32_bf16 v[26:29], v[142:145], v[188:191], v[26:29]
	v_mfma_f32_16x16x32_bf16 v[14:17], v[134:137], v[196:199], v[14:17]
	v_mfma_f32_16x16x32_bf16 v[10:13], v[142:145], v[196:199], v[10:13]
	s_setprio 0
	s_barrier
	s_add_u32 s56, s36, 0x80000
	s_addc_u32 s57, s37, 0
	s_add_i32 s58, s49, s5
	v_lshl_add_u64 v[130:131], s[56:57], 0, v[148:149]
	s_mov_b32 m0, s58
	s_nop 0
	global_load_lds_dwordx4 v[130:131], off
	v_lshl_add_u64 v[130:131], s[56:57], 0, v[152:153]
	s_add_i32 m0, s58, 0x2000
	s_nop 0
	global_load_lds_dwordx4 v[130:131], off
	s_waitcnt vmcnt(6)
	s_barrier
	s_setprio 1
	v_mfma_f32_16x16x32_bf16 v[54:57], v[200:203], v[162:165], 0
	v_mfma_f32_16x16x32_bf16 v[50:53], v[208:211], v[162:165], 0
	ds_read_b128 v[162:165], v173 offset:32768
	v_mfma_f32_16x16x32_bf16 v[38:41], v[200:203], v[176:179], 0
	v_mfma_f32_16x16x32_bf16 v[34:37], v[208:211], v[176:179], 0
	ds_read_b128 v[176:179], v173 offset:34816
	v_mfma_f32_16x16x32_bf16 v[22:25], v[200:203], v[184:187], 0
	v_mfma_f32_16x16x32_bf16 v[18:21], v[208:211], v[184:187], 0
	ds_read_b128 v[184:187], v173 offset:36864
	v_mfma_f32_16x16x32_bf16 v[6:9], v[200:203], v[192:195], 0
	v_mfma_f32_16x16x32_bf16 v[2:5], v[208:211], v[192:195], 0
	ds_read_b128 v[192:195], v173 offset:38912
	v_mfma_f32_16x16x32_bf16 v[54:57], v[204:207], v[166:169], v[54:57]
	v_mfma_f32_16x16x32_bf16 v[50:53], v[214:217], v[166:169], v[50:53]
	ds_read_b128 v[166:169], v173 offset:33792
	v_mfma_f32_16x16x32_bf16 v[38:41], v[204:207], v[180:183], v[38:41]
	v_mfma_f32_16x16x32_bf16 v[34:37], v[214:217], v[180:183], v[34:37]
	ds_read_b128 v[180:183], v173 offset:35840
	v_mfma_f32_16x16x32_bf16 v[22:25], v[204:207], v[188:191], v[22:25]
	v_mfma_f32_16x16x32_bf16 v[18:21], v[214:217], v[188:191], v[18:21]
	ds_read_b128 v[188:191], v173 offset:37888
	v_mfma_f32_16x16x32_bf16 v[6:9], v[204:207], v[196:199], v[6:9]
	v_mfma_f32_16x16x32_bf16 v[2:5], v[214:217], v[196:199], v[2:5]
	ds_read_b128 v[196:199], v173 offset:39936
	s_setprio 0
	s_add_i32 s56, 0, 0x18000
	v_add_u32_e32 v142, s56, v171
	s_barrier
	ds_read_b128 v[130:133], v142
	ds_read_b128 v[134:137], v142 offset:1024
	ds_read_b128 v[138:141], v142 offset:2048
	ds_read_b128 v[142:145], v142 offset:3072
	s_add_u32 s38, s38, 0x80000
	s_addc_u32 s39, s39, 0
	s_mov_b32 m0, s35
	v_lshl_add_u64 v[200:201], s[38:39], 0, v[146:147]
	global_load_lds_dwordx4 v[200:201], off
	v_lshl_add_u64 v[200:201], s[38:39], 0, v[150:151]
	s_mov_b32 m0, s40
	s_nop 0
	global_load_lds_dwordx4 v[200:201], off
	s_waitcnt lgkmcnt(8)
	s_barrier
	s_waitcnt lgkmcnt(0)
	s_setprio 1
	s_waitcnt lgkmcnt(0)
	v_mfma_f32_16x16x32_bf16 v[126:129], v[130:133], v[162:165], v[126:129]
	v_mfma_f32_16x16x32_bf16 v[122:125], v[138:141], v[162:165], v[122:125]
	v_mfma_f32_16x16x32_bf16 v[110:113], v[130:133], v[176:179], v[110:113]
	v_mfma_f32_16x16x32_bf16 v[106:109], v[138:141], v[176:179], v[106:109]
	v_mfma_f32_16x16x32_bf16 v[94:97], v[130:133], v[184:187], v[94:97]
	v_mfma_f32_16x16x32_bf16 v[90:93], v[138:141], v[184:187], v[90:93]
	v_mfma_f32_16x16x32_bf16 v[78:81], v[130:133], v[192:195], v[78:81]
	v_mfma_f32_16x16x32_bf16 v[74:77], v[138:141], v[192:195], v[74:77]
	v_mfma_f32_16x16x32_bf16 v[126:129], v[134:137], v[166:169], v[126:129]
	v_mfma_f32_16x16x32_bf16 v[122:125], v[142:145], v[166:169], v[122:125]
	v_mfma_f32_16x16x32_bf16 v[110:113], v[134:137], v[180:183], v[110:113]
	v_mfma_f32_16x16x32_bf16 v[106:109], v[142:145], v[180:183], v[106:109]
	v_mfma_f32_16x16x32_bf16 v[94:97], v[134:137], v[188:191], v[94:97]
	v_mfma_f32_16x16x32_bf16 v[90:93], v[142:145], v[188:191], v[90:93]
	v_mfma_f32_16x16x32_bf16 v[78:81], v[134:137], v[196:199], v[78:81]
	v_mfma_f32_16x16x32_bf16 v[74:77], v[142:145], v[196:199], v[74:77]
	s_setprio 0
	s_barrier
	s_add_i32 s38, 0, 0x1c000
	s_add_i32 s39, s56, s5
	v_add_u32_e32 v175, s38, v171
	v_lshl_add_u64 v[218:219], v[218:219], 0, s[18:19]
	s_mov_b32 m0, s39
	ds_read_b128 v[200:203], v175
	ds_read_b128 v[204:207], v175 offset:1024
	ds_read_b128 v[208:211], v175 offset:2048
	ds_read_b128 v[214:217], v175 offset:3072
	global_load_lds_dwordx4 v[218:219], off
	v_lshl_add_u64 v[218:219], v[220:221], 0, s[18:19]
	s_add_i32 m0, s39, 0x2000
	s_nop 0
	global_load_lds_dwordx4 v[218:219], off
	s_barrier
	s_waitcnt lgkmcnt(0)
	s_setprio 1
	s_waitcnt lgkmcnt(0)
	v_mfma_f32_16x16x32_bf16 v[118:121], v[200:203], v[162:165], v[118:121]
	v_mfma_f32_16x16x32_bf16 v[114:117], v[208:211], v[162:165], v[114:117]
	ds_read_b128 v[162:165], v173 offset:49152
	v_mfma_f32_16x16x32_bf16 v[102:105], v[200:203], v[176:179], v[102:105]
	v_mfma_f32_16x16x32_bf16 v[98:101], v[208:211], v[176:179], v[98:101]
	ds_read_b128 v[176:179], v173 offset:51200
	v_mfma_f32_16x16x32_bf16 v[86:89], v[200:203], v[184:187], v[86:89]
	v_mfma_f32_16x16x32_bf16 v[82:85], v[208:211], v[184:187], v[82:85]
	ds_read_b128 v[184:187], v173 offset:53248
	v_mfma_f32_16x16x32_bf16 v[70:73], v[200:203], v[192:195], v[70:73]
	v_mfma_f32_16x16x32_bf16 v[66:69], v[208:211], v[192:195], v[66:69]
	ds_read_b128 v[192:195], v173 offset:55296
	v_mfma_f32_16x16x32_bf16 v[118:121], v[204:207], v[166:169], v[118:121]
	v_mfma_f32_16x16x32_bf16 v[114:117], v[214:217], v[166:169], v[114:117]
	ds_read_b128 v[166:169], v173 offset:50176
	v_mfma_f32_16x16x32_bf16 v[102:105], v[204:207], v[180:183], v[102:105]
	v_mfma_f32_16x16x32_bf16 v[98:101], v[214:217], v[180:183], v[98:101]
	ds_read_b128 v[180:183], v173 offset:52224
	v_mfma_f32_16x16x32_bf16 v[86:89], v[204:207], v[188:191], v[86:89]
	v_mfma_f32_16x16x32_bf16 v[82:85], v[214:217], v[188:191], v[82:85]
	ds_read_b128 v[188:191], v173 offset:54272
	v_mfma_f32_16x16x32_bf16 v[70:73], v[204:207], v[196:199], v[70:73]
	v_mfma_f32_16x16x32_bf16 v[66:69], v[214:217], v[196:199], v[66:69]
	ds_read_b128 v[196:199], v173 offset:56320
	s_setprio 0
	s_mov_b32 m0, s44
	v_lshl_add_u64 v[218:219], v[222:223], 0, s[18:19]
	s_barrier
	global_load_lds_dwordx4 v[218:219], off
	v_lshl_add_u64 v[218:219], v[224:225], 0, s[18:19]
	s_mov_b32 m0, s45
	s_nop 0
	global_load_lds_dwordx4 v[218:219], off
	s_barrier
	s_waitcnt lgkmcnt(0)
	s_setprio 1
	s_waitcnt lgkmcnt(0)
	v_mfma_f32_16x16x32_bf16 v[62:65], v[130:133], v[162:165], v[62:65]
	v_mfma_f32_16x16x32_bf16 v[58:61], v[138:141], v[162:165], v[58:61]
	v_mfma_f32_16x16x32_bf16 v[46:49], v[130:133], v[176:179], v[46:49]
	v_mfma_f32_16x16x32_bf16 v[42:45], v[138:141], v[176:179], v[42:45]
	v_mfma_f32_16x16x32_bf16 v[30:33], v[130:133], v[184:187], v[30:33]
	v_mfma_f32_16x16x32_bf16 v[26:29], v[138:141], v[184:187], v[26:29]
	v_mfma_f32_16x16x32_bf16 v[14:17], v[130:133], v[192:195], v[14:17]
	v_mfma_f32_16x16x32_bf16 v[10:13], v[138:141], v[192:195], v[10:13]
	v_mfma_f32_16x16x32_bf16 v[62:65], v[134:137], v[166:169], v[62:65]
	v_mfma_f32_16x16x32_bf16 v[58:61], v[142:145], v[166:169], v[58:61]
	v_mfma_f32_16x16x32_bf16 v[46:49], v[134:137], v[180:183], v[46:49]
	v_mfma_f32_16x16x32_bf16 v[42:45], v[142:145], v[180:183], v[42:45]
	v_mfma_f32_16x16x32_bf16 v[30:33], v[134:137], v[188:191], v[30:33]
	v_mfma_f32_16x16x32_bf16 v[26:29], v[142:145], v[188:191], v[26:29]
	v_mfma_f32_16x16x32_bf16 v[14:17], v[134:137], v[196:199], v[14:17]
	v_mfma_f32_16x16x32_bf16 v[10:13], v[142:145], v[196:199], v[10:13]
	s_setprio 0
	s_barrier
	s_add_u32 s36, s36, 0x80080
	s_addc_u32 s37, s37, 0
	s_add_i32 s38, s38, s5
	v_lshl_add_u64 v[130:131], s[36:37], 0, v[148:149]
	s_mov_b32 m0, s38
	s_nop 0
	global_load_lds_dwordx4 v[130:131], off
	v_lshl_add_u64 v[130:131], s[36:37], 0, v[152:153]
	s_add_i32 m0, s38, 0x2000
	s_nop 0
	global_load_lds_dwordx4 v[130:131], off
	s_waitcnt vmcnt(6)
	s_barrier
	s_setprio 1
	v_mfma_f32_16x16x32_bf16 v[54:57], v[200:203], v[162:165], v[54:57]
	v_mfma_f32_16x16x32_bf16 v[50:53], v[208:211], v[162:165], v[50:53]
	v_mfma_f32_16x16x32_bf16 v[38:41], v[200:203], v[176:179], v[38:41]
	v_mfma_f32_16x16x32_bf16 v[34:37], v[208:211], v[176:179], v[34:37]
	v_mfma_f32_16x16x32_bf16 v[22:25], v[200:203], v[184:187], v[22:25]
	v_mfma_f32_16x16x32_bf16 v[18:21], v[208:211], v[184:187], v[18:21]
	v_mfma_f32_16x16x32_bf16 v[6:9], v[200:203], v[192:195], v[6:9]
	v_mfma_f32_16x16x32_bf16 v[2:5], v[208:211], v[192:195], v[2:5]
	v_mfma_f32_16x16x32_bf16 v[54:57], v[204:207], v[166:169], v[54:57]
	v_mfma_f32_16x16x32_bf16 v[50:53], v[214:217], v[166:169], v[50:53]
	v_mfma_f32_16x16x32_bf16 v[38:41], v[204:207], v[180:183], v[38:41]
	v_mfma_f32_16x16x32_bf16 v[34:37], v[214:217], v[180:183], v[34:37]
	v_mfma_f32_16x16x32_bf16 v[22:25], v[204:207], v[188:191], v[22:25]
	v_mfma_f32_16x16x32_bf16 v[18:21], v[214:217], v[188:191], v[18:21]
	v_mfma_f32_16x16x32_bf16 v[6:9], v[204:207], v[196:199], v[6:9]
	v_mfma_f32_16x16x32_bf16 v[2:5], v[214:217], v[196:199], v[2:5]
	s_setprio 0
	s_add_u32 s8, s8, 0x100
	s_addc_u32 s9, s9, 0
	s_add_u32 s53, s53, 0x100
	s_addc_u32 s54, s54, 0
	s_cmp_ge_i32 s55, s1
	s_mov_b32 s36, s55
	s_barrier
	s_cbranch_scc0 .LBB0_964
	s_branch .Lmy_pl1_exit
.LBB0_964:
	ds_read_b128 v[130:133], v172
	ds_read_b128 v[134:137], v172 offset:1024
	ds_read_b128 v[138:141], v172 offset:2048
	ds_read_b128 v[142:145], v172 offset:3072
	s_add_i32 s55, s36, 2
	s_add_u32 s37, s8, 0xfff80080
	s_addc_u32 s38, s9, -1
	s_cmp_eq_u32 s46, s36
	s_cselect_b32 s36, s52, s53
	s_cselect_b32 s39, s25, s38
	s_cselect_b32 s38, s27, s37
	s_cselect_b32 s37, s51, s54
	v_lshl_add_u64 v[200:201], s[8:9], 0, v[154:155]
	s_add_i32 m0, s23, 0xc000
	ds_read_b128 v[162:165], v173
	ds_read_b128 v[166:169], v173 offset:1024
	ds_read_b128 v[176:179], v173 offset:2048
	ds_read_b128 v[180:183], v173 offset:3072
	ds_read_b128 v[184:187], v173 offset:4096
	ds_read_b128 v[188:191], v173 offset:5120
	ds_read_b128 v[192:195], v173 offset:6144
	ds_read_b128 v[196:199], v173 offset:7168
	global_load_lds_dwordx4 v[200:201], off
	v_lshl_add_u64 v[200:201], s[8:9], 0, v[156:157]
	s_add_i32 m0, s23, 0xe000
	s_nop 0
	global_load_lds_dwordx4 v[200:201], off
	s_waitcnt lgkmcnt(8)
	s_barrier
	s_waitcnt lgkmcnt(0)
	s_setprio 1
	s_waitcnt lgkmcnt(0)
	v_mfma_f32_16x16x32_bf16 v[126:129], v[130:133], v[162:165], v[126:129]
	ds_read_b128 v[200:203], v174
	ds_read_b128 v[204:207], v174 offset:1024
	ds_read_b128 v[208:211], v174 offset:2048
	ds_read_b128 v[214:217], v174 offset:3072
	v_mfma_f32_16x16x32_bf16 v[122:125], v[138:141], v[162:165], v[122:125]
	v_mfma_f32_16x16x32_bf16 v[110:113], v[130:133], v[176:179], v[110:113]
	v_mfma_f32_16x16x32_bf16 v[106:109], v[138:141], v[176:179], v[106:109]
	v_mfma_f32_16x16x32_bf16 v[94:97], v[130:133], v[184:187], v[94:97]
	v_mfma_f32_16x16x32_bf16 v[90:93], v[138:141], v[184:187], v[90:93]
	v_mfma_f32_16x16x32_bf16 v[78:81], v[130:133], v[192:195], v[78:81]
	v_mfma_f32_16x16x32_bf16 v[74:77], v[138:141], v[192:195], v[74:77]
	v_mfma_f32_16x16x32_bf16 v[126:129], v[134:137], v[166:169], v[126:129]
	v_mfma_f32_16x16x32_bf16 v[122:125], v[142:145], v[166:169], v[122:125]
	v_mfma_f32_16x16x32_bf16 v[110:113], v[134:137], v[180:183], v[110:113]
	v_mfma_f32_16x16x32_bf16 v[106:109], v[142:145], v[180:183], v[106:109]
	v_mfma_f32_16x16x32_bf16 v[94:97], v[134:137], v[188:191], v[94:97]
	v_mfma_f32_16x16x32_bf16 v[90:93], v[142:145], v[188:191], v[90:93]
	v_mfma_f32_16x16x32_bf16 v[78:81], v[134:137], v[196:199], v[78:81]
	v_mfma_f32_16x16x32_bf16 v[74:77], v[142:145], v[196:199], v[74:77]
	s_setprio 0
	s_barrier
	s_add_i32 s56, s48, s5
	v_lshl_add_u64 v[218:219], s[36:37], 0, v[148:149]
	s_mov_b32 m0, s56
	global_load_lds_dwordx4 v[218:219], off
	v_lshl_add_u64 v[220:221], s[36:37], 0, v[152:153]
	s_add_i32 m0, s56, 0x2000
	s_nop 0
	global_load_lds_dwordx4 v[220:221], off
	s_barrier
	s_waitcnt lgkmcnt(0)
	s_setprio 1
	s_waitcnt lgkmcnt(0)
	v_mfma_f32_16x16x32_bf16 v[118:121], v[200:203], v[162:165], v[118:121]
	v_mfma_f32_16x16x32_bf16 v[114:117], v[208:211], v[162:165], v[114:117]
	ds_read_b128 v[162:165], v173 offset:16384
	v_mfma_f32_16x16x32_bf16 v[102:105], v[200:203], v[176:179], v[102:105]
	v_mfma_f32_16x16x32_bf16 v[98:101], v[208:211], v[176:179], v[98:101]
	ds_read_b128 v[176:179], v173 offset:18432
	v_mfma_f32_16x16x32_bf16 v[86:89], v[200:203], v[184:187], v[86:89]
	v_mfma_f32_16x16x32_bf16 v[82:85], v[208:211], v[184:187], v[82:85]
	ds_read_b128 v[184:187], v173 offset:20480
	v_mfma_f32_16x16x32_bf16 v[70:73], v[200:203], v[192:195], v[70:73]
	v_mfma_f32_16x16x32_bf16 v[66:69], v[208:211], v[192:195], v[66:69]
	ds_read_b128 v[192:195], v173 offset:22528
	v_mfma_f32_16x16x32_bf16 v[118:121], v[204:207], v[166:169], v[118:121]
	v_mfma_f32_16x16x32_bf16 v[114:117], v[214:217], v[166:169], v[114:117]
	ds_read_b128 v[166:169], v173 offset:17408
	v_mfma_f32_16x16x32_bf16 v[102:105], v[204:207], v[180:183], v[102:105]
	v_mfma_f32_16x16x32_bf16 v[98:101], v[214:217], v[180:183], v[98:101]
	ds_read_b128 v[180:183], v173 offset:19456
	v_mfma_f32_16x16x32_bf16 v[86:89], v[204:207], v[188:191], v[86:89]
	v_mfma_f32_16x16x32_bf16 v[82:85], v[214:217], v[188:191], v[82:85]
	ds_read_b128 v[188:191], v173 offset:21504
	v_mfma_f32_16x16x32_bf16 v[70:73], v[204:207], v[196:199], v[70:73]
	v_mfma_f32_16x16x32_bf16 v[66:69], v[214:217], v[196:199], v[66:69]
	ds_read_b128 v[196:199], v173 offset:23552
	s_setprio 0
	s_mov_b32 m0, s23
	v_lshl_add_u64 v[222:223], s[38:39], 0, v[146:147]
	s_barrier
	global_load_lds_dwordx4 v[222:223], off
	v_lshl_add_u64 v[224:225], s[38:39], 0, v[150:151]
	s_mov_b32 m0, s33
	s_nop 0
	global_load_lds_dwordx4 v[224:225], off
	s_barrier
	s_waitcnt lgkmcnt(0)
	s_setprio 1
	s_waitcnt lgkmcnt(0)
	v_mfma_f32_16x16x32_bf16 v[62:65], v[130:133], v[162:165], v[62:65]
	v_mfma_f32_16x16x32_bf16 v[58:61], v[138:141], v[162:165], v[58:61]
	v_mfma_f32_16x16x32_bf16 v[46:49], v[130:133], v[176:179], v[46:49]
	v_mfma_f32_16x16x32_bf16 v[42:45], v[138:141], v[176:179], v[42:45]
	v_mfma_f32_16x16x32_bf16 v[30:33], v[130:133], v[184:187], v[30:33]
	v_mfma_f32_16x16x32_bf16 v[26:29], v[138:141], v[184:187], v[26:29]
	v_mfma_f32_16x16x32_bf16 v[14:17], v[130:133], v[192:195], v[14:17]
	v_mfma_f32_16x16x32_bf16 v[10:13], v[138:141], v[192:195], v[10:13]
	v_mfma_f32_16x16x32_bf16 v[62:65], v[134:137], v[166:169], v[62:65]
	v_mfma_f32_16x16x32_bf16 v[58:61], v[142:145], v[166:169], v[58:61]
	v_mfma_f32_16x16x32_bf16 v[46:49], v[134:137], v[180:183], v[46:49]
	v_mfma_f32_16x16x32_bf16 v[42:45], v[142:145], v[180:183], v[42:45]
	v_mfma_f32_16x16x32_bf16 v[30:33], v[134:137], v[188:191], v[30:33]
	v_mfma_f32_16x16x32_bf16 v[26:29], v[142:145], v[188:191], v[26:29]
	v_mfma_f32_16x16x32_bf16 v[14:17], v[134:137], v[196:199], v[14:17]
	v_mfma_f32_16x16x32_bf16 v[10:13], v[142:145], v[196:199], v[10:13]
	s_setprio 0
	s_barrier
	s_add_u32 s56, s36, 0x80000
	s_addc_u32 s57, s37, 0
	s_add_i32 s58, s49, s5
	v_lshl_add_u64 v[130:131], s[56:57], 0, v[148:149]
	s_mov_b32 m0, s58
	s_nop 0
	global_load_lds_dwordx4 v[130:131], off
	v_lshl_add_u64 v[130:131], s[56:57], 0, v[152:153]
	s_add_i32 m0, s58, 0x2000
	s_nop 0
	global_load_lds_dwordx4 v[130:131], off
	s_waitcnt vmcnt(6)
	s_barrier
	s_setprio 1
	v_mfma_f32_16x16x32_bf16 v[54:57], v[200:203], v[162:165], v[54:57]
	v_mfma_f32_16x16x32_bf16 v[50:53], v[208:211], v[162:165], v[50:53]
	ds_read_b128 v[162:165], v173 offset:32768
	v_mfma_f32_16x16x32_bf16 v[38:41], v[200:203], v[176:179], v[38:41]
	v_mfma_f32_16x16x32_bf16 v[34:37], v[208:211], v[176:179], v[34:37]
	ds_read_b128 v[176:179], v173 offset:34816
	v_mfma_f32_16x16x32_bf16 v[22:25], v[200:203], v[184:187], v[22:25]
	v_mfma_f32_16x16x32_bf16 v[18:21], v[208:211], v[184:187], v[18:21]
	ds_read_b128 v[184:187], v173 offset:36864
	v_mfma_f32_16x16x32_bf16 v[6:9], v[200:203], v[192:195], v[6:9]
	v_mfma_f32_16x16x32_bf16 v[2:5], v[208:211], v[192:195], v[2:5]
	ds_read_b128 v[192:195], v173 offset:38912
	v_mfma_f32_16x16x32_bf16 v[54:57], v[204:207], v[166:169], v[54:57]
	v_mfma_f32_16x16x32_bf16 v[50:53], v[214:217], v[166:169], v[50:53]
	ds_read_b128 v[166:169], v173 offset:33792
	v_mfma_f32_16x16x32_bf16 v[38:41], v[204:207], v[180:183], v[38:41]
	v_mfma_f32_16x16x32_bf16 v[34:37], v[214:217], v[180:183], v[34:37]
	ds_read_b128 v[180:183], v173 offset:35840
	v_mfma_f32_16x16x32_bf16 v[22:25], v[204:207], v[188:191], v[22:25]
	v_mfma_f32_16x16x32_bf16 v[18:21], v[214:217], v[188:191], v[18:21]
	ds_read_b128 v[188:191], v173 offset:37888
	v_mfma_f32_16x16x32_bf16 v[6:9], v[204:207], v[196:199], v[6:9]
	v_mfma_f32_16x16x32_bf16 v[2:5], v[214:217], v[196:199], v[2:5]
	ds_read_b128 v[196:199], v173 offset:39936
	s_setprio 0
	s_add_i32 s56, 0, 0x18000
	v_add_u32_e32 v142, s56, v171
	s_barrier
	ds_read_b128 v[130:133], v142
	ds_read_b128 v[134:137], v142 offset:1024
	ds_read_b128 v[138:141], v142 offset:2048
	ds_read_b128 v[142:145], v142 offset:3072
	s_add_u32 s38, s38, 0x80000
	s_addc_u32 s39, s39, 0
	s_mov_b32 m0, s35
	v_lshl_add_u64 v[200:201], s[38:39], 0, v[146:147]
	global_load_lds_dwordx4 v[200:201], off
	v_lshl_add_u64 v[200:201], s[38:39], 0, v[150:151]
	s_mov_b32 m0, s40
	s_nop 0
	global_load_lds_dwordx4 v[200:201], off
	s_waitcnt lgkmcnt(8)
	s_barrier
	s_waitcnt lgkmcnt(0)
	s_setprio 1
	s_waitcnt lgkmcnt(0)
	v_mfma_f32_16x16x32_bf16 v[126:129], v[130:133], v[162:165], v[126:129]
	v_mfma_f32_16x16x32_bf16 v[122:125], v[138:141], v[162:165], v[122:125]
	v_mfma_f32_16x16x32_bf16 v[110:113], v[130:133], v[176:179], v[110:113]
	v_mfma_f32_16x16x32_bf16 v[106:109], v[138:141], v[176:179], v[106:109]
	v_mfma_f32_16x16x32_bf16 v[94:97], v[130:133], v[184:187], v[94:97]
	v_mfma_f32_16x16x32_bf16 v[90:93], v[138:141], v[184:187], v[90:93]
	v_mfma_f32_16x16x32_bf16 v[78:81], v[130:133], v[192:195], v[78:81]
	v_mfma_f32_16x16x32_bf16 v[74:77], v[138:141], v[192:195], v[74:77]
	v_mfma_f32_16x16x32_bf16 v[126:129], v[134:137], v[166:169], v[126:129]
	v_mfma_f32_16x16x32_bf16 v[122:125], v[142:145], v[166:169], v[122:125]
	v_mfma_f32_16x16x32_bf16 v[110:113], v[134:137], v[180:183], v[110:113]
	v_mfma_f32_16x16x32_bf16 v[106:109], v[142:145], v[180:183], v[106:109]
	v_mfma_f32_16x16x32_bf16 v[94:97], v[134:137], v[188:191], v[94:97]
	v_mfma_f32_16x16x32_bf16 v[90:93], v[142:145], v[188:191], v[90:93]
	v_mfma_f32_16x16x32_bf16 v[78:81], v[134:137], v[196:199], v[78:81]
	v_mfma_f32_16x16x32_bf16 v[74:77], v[142:145], v[196:199], v[74:77]
	s_setprio 0
	s_barrier
	s_add_i32 s38, 0, 0x1c000
	s_add_i32 s39, s56, s5
	v_add_u32_e32 v175, s38, v171
	v_lshl_add_u64 v[218:219], v[218:219], 0, s[18:19]
	s_mov_b32 m0, s39
	ds_read_b128 v[200:203], v175
	ds_read_b128 v[204:207], v175 offset:1024
	ds_read_b128 v[208:211], v175 offset:2048
	ds_read_b128 v[214:217], v175 offset:3072
	global_load_lds_dwordx4 v[218:219], off
	v_lshl_add_u64 v[218:219], v[220:221], 0, s[18:19]
	s_add_i32 m0, s39, 0x2000
	s_nop 0
	global_load_lds_dwordx4 v[218:219], off
	s_barrier
	s_waitcnt lgkmcnt(0)
	s_setprio 1
	s_waitcnt lgkmcnt(0)
	v_mfma_f32_16x16x32_bf16 v[118:121], v[200:203], v[162:165], v[118:121]
	v_mfma_f32_16x16x32_bf16 v[114:117], v[208:211], v[162:165], v[114:117]
	ds_read_b128 v[162:165], v173 offset:49152
	v_mfma_f32_16x16x32_bf16 v[102:105], v[200:203], v[176:179], v[102:105]
	v_mfma_f32_16x16x32_bf16 v[98:101], v[208:211], v[176:179], v[98:101]
	ds_read_b128 v[176:179], v173 offset:51200
	v_mfma_f32_16x16x32_bf16 v[86:89], v[200:203], v[184:187], v[86:89]
	v_mfma_f32_16x16x32_bf16 v[82:85], v[208:211], v[184:187], v[82:85]
	ds_read_b128 v[184:187], v173 offset:53248
	v_mfma_f32_16x16x32_bf16 v[70:73], v[200:203], v[192:195], v[70:73]
	v_mfma_f32_16x16x32_bf16 v[66:69], v[208:211], v[192:195], v[66:69]
	ds_read_b128 v[192:195], v173 offset:55296
	v_mfma_f32_16x16x32_bf16 v[118:121], v[204:207], v[166:169], v[118:121]
	v_mfma_f32_16x16x32_bf16 v[114:117], v[214:217], v[166:169], v[114:117]
	ds_read_b128 v[166:169], v173 offset:50176
	v_mfma_f32_16x16x32_bf16 v[102:105], v[204:207], v[180:183], v[102:105]
	v_mfma_f32_16x16x32_bf16 v[98:101], v[214:217], v[180:183], v[98:101]
	ds_read_b128 v[180:183], v173 offset:52224
	v_mfma_f32_16x16x32_bf16 v[86:89], v[204:207], v[188:191], v[86:89]
	v_mfma_f32_16x16x32_bf16 v[82:85], v[214:217], v[188:191], v[82:85]
	ds_read_b128 v[188:191], v173 offset:54272
	v_mfma_f32_16x16x32_bf16 v[70:73], v[204:207], v[196:199], v[70:73]
	v_mfma_f32_16x16x32_bf16 v[66:69], v[214:217], v[196:199], v[66:69]
	ds_read_b128 v[196:199], v173 offset:56320
	s_setprio 0
	s_mov_b32 m0, s44
	v_lshl_add_u64 v[218:219], v[222:223], 0, s[18:19]
	s_barrier
	global_load_lds_dwordx4 v[218:219], off
	v_lshl_add_u64 v[218:219], v[224:225], 0, s[18:19]
	s_mov_b32 m0, s45
	s_nop 0
	global_load_lds_dwordx4 v[218:219], off
	s_barrier
	s_waitcnt lgkmcnt(0)
	s_setprio 1
	s_waitcnt lgkmcnt(0)
	v_mfma_f32_16x16x32_bf16 v[62:65], v[130:133], v[162:165], v[62:65]
	v_mfma_f32_16x16x32_bf16 v[58:61], v[138:141], v[162:165], v[58:61]
	v_mfma_f32_16x16x32_bf16 v[46:49], v[130:133], v[176:179], v[46:49]
	v_mfma_f32_16x16x32_bf16 v[42:45], v[138:141], v[176:179], v[42:45]
	v_mfma_f32_16x16x32_bf16 v[30:33], v[130:133], v[184:187], v[30:33]
	v_mfma_f32_16x16x32_bf16 v[26:29], v[138:141], v[184:187], v[26:29]
	v_mfma_f32_16x16x32_bf16 v[14:17], v[130:133], v[192:195], v[14:17]
	v_mfma_f32_16x16x32_bf16 v[10:13], v[138:141], v[192:195], v[10:13]
	v_mfma_f32_16x16x32_bf16 v[62:65], v[134:137], v[166:169], v[62:65]
	v_mfma_f32_16x16x32_bf16 v[58:61], v[142:145], v[166:169], v[58:61]
	v_mfma_f32_16x16x32_bf16 v[46:49], v[134:137], v[180:183], v[46:49]
	v_mfma_f32_16x16x32_bf16 v[42:45], v[142:145], v[180:183], v[42:45]
	v_mfma_f32_16x16x32_bf16 v[30:33], v[134:137], v[188:191], v[30:33]
	v_mfma_f32_16x16x32_bf16 v[26:29], v[142:145], v[188:191], v[26:29]
	v_mfma_f32_16x16x32_bf16 v[14:17], v[134:137], v[196:199], v[14:17]
	v_mfma_f32_16x16x32_bf16 v[10:13], v[142:145], v[196:199], v[10:13]
	s_setprio 0
	s_barrier
	s_add_u32 s36, s36, 0x80080
	s_addc_u32 s37, s37, 0
	s_add_i32 s38, s38, s5
	v_lshl_add_u64 v[130:131], s[36:37], 0, v[148:149]
	s_mov_b32 m0, s38
	s_nop 0
	global_load_lds_dwordx4 v[130:131], off
	v_lshl_add_u64 v[130:131], s[36:37], 0, v[152:153]
	s_add_i32 m0, s38, 0x2000
	s_nop 0
	global_load_lds_dwordx4 v[130:131], off
	s_waitcnt vmcnt(6)
	s_barrier
	s_setprio 1
	v_mfma_f32_16x16x32_bf16 v[54:57], v[200:203], v[162:165], v[54:57]
	v_mfma_f32_16x16x32_bf16 v[50:53], v[208:211], v[162:165], v[50:53]
	v_mfma_f32_16x16x32_bf16 v[38:41], v[200:203], v[176:179], v[38:41]
	v_mfma_f32_16x16x32_bf16 v[34:37], v[208:211], v[176:179], v[34:37]
	v_mfma_f32_16x16x32_bf16 v[22:25], v[200:203], v[184:187], v[22:25]
	v_mfma_f32_16x16x32_bf16 v[18:21], v[208:211], v[184:187], v[18:21]
	v_mfma_f32_16x16x32_bf16 v[6:9], v[200:203], v[192:195], v[6:9]
	v_mfma_f32_16x16x32_bf16 v[2:5], v[208:211], v[192:195], v[2:5]
	v_mfma_f32_16x16x32_bf16 v[54:57], v[204:207], v[166:169], v[54:57]
	v_mfma_f32_16x16x32_bf16 v[50:53], v[214:217], v[166:169], v[50:53]
	v_mfma_f32_16x16x32_bf16 v[38:41], v[204:207], v[180:183], v[38:41]
	v_mfma_f32_16x16x32_bf16 v[34:37], v[214:217], v[180:183], v[34:37]
	v_mfma_f32_16x16x32_bf16 v[22:25], v[204:207], v[188:191], v[22:25]
	v_mfma_f32_16x16x32_bf16 v[18:21], v[214:217], v[188:191], v[18:21]
	v_mfma_f32_16x16x32_bf16 v[6:9], v[204:207], v[196:199], v[6:9]
	v_mfma_f32_16x16x32_bf16 v[2:5], v[214:217], v[196:199], v[2:5]
	s_setprio 0
	s_add_u32 s8, s8, 0x100
	s_addc_u32 s9, s9, 0
	s_add_u32 s53, s53, 0x100
	s_addc_u32 s54, s54, 0
	s_cmp_ge_i32 s55, s1
	s_mov_b32 s36, s55
	s_barrier
	s_cbranch_scc0 .LBB0_964

.Lmy_pl2_1553:
	s_add_i32 s71, s71, 2
	s_add_u32 s30, s28, 0x100
	s_addc_u32 s31, s29, 0
	s_and_b64 s[36:37], s[34:35], exec
	s_cselect_b32 s36, 0, s30
	s_cselect_b32 s37, 0, s31
	s_add_u32 s36, s22, s36
	s_addc_u32 s37, s23, s37
	s_add_u32 s72, s69, s28
	s_addc_u32 s73, s70, s29
	s_and_b64 s[28:29], s[34:35], exec
	s_cselect_b32 s29, s67, s73
	s_cselect_b32 s28, s68, s72
	s_mov_b32 m0, s42
	v_add_u32_e32 v191, s57, v204
	v_lshl_add_u64 v[230:231], s[28:29], 0, v[188:189]
	v_add_u32_e32 v197, s57, v205
	ds_read_b128 v[214:217], v191
	ds_read_b128 v[222:225], v191 offset:2048
	ds_read_b128 v[218:221], v197
	ds_read_b128 v[226:229], v197 offset:2048
	global_load_lds_dwordx4 v[230:231], off
	v_lshl_add_u64 v[232:233], s[28:29], 0, v[186:187]
	s_mov_b32 m0, s43
	s_waitcnt lgkmcnt(0)
	v_mfma_scale_f32_16x16x128_f8f6f4 v[174:177], v[2:9], v[26:33], 0, v211, v210 op_sel_hi:[0,0,0]
	global_load_lds_dwordx4 v[232:233], off
	s_barrier
	s_waitcnt lgkmcnt(0)
	v_mov_b32_e32 v193, v185
	v_mov_b32_e32 v195, v185
	v_mfma_scale_f32_16x16x128_f8f6f4 v[170:173], v[10:17], v[26:33], 0, v211, v210 op_sel_hi:[0,0,0]
	v_mfma_scale_f32_16x16x128_f8f6f4 v[166:169], v[2:9], v[18:25], 0, v211, v210 op_sel_hi:[0,0,0]
	v_mfma_scale_f32_16x16x128_f8f6f4 v[162:165], v[10:17], v[18:25], 0, v211, v210 op_sel_hi:[0,0,0]
	v_mfma_scale_f32_16x16x128_f8f6f4 v[142:145], v[2:9], v[42:49], 0, v211, v210 op_sel_hi:[0,0,0]
	v_mfma_scale_f32_16x16x128_f8f6f4 v[130:133], v[10:17], v[42:49], 0, v211, v210 op_sel_hi:[0,0,0]
	v_mfma_scale_f32_16x16x128_f8f6f4 v[118:121], v[2:9], v[34:41], 0, v211, v210 op_sel_hi:[0,0,0]
	v_mfma_scale_f32_16x16x128_f8f6f4 v[114:117], v[10:17], v[34:41], 0, v211, v210 op_sel_hi:[0,0,0]
	s_setprio 1
	v_mfma_scale_f32_16x16x128_f8f6f4 v[158:161], v[214:221], v[26:33], 0, v211, v210 op_sel_hi:[0,0,0]
	v_mfma_scale_f32_16x16x128_f8f6f4 v[154:157], v[222:229], v[26:33], 0, v211, v210 op_sel_hi:[0,0,0]
	ds_read_b128 v[26:29], v208 offset:18432
	ds_read_b128 v[30:33], v209 offset:18432
	v_mfma_scale_f32_16x16x128_f8f6f4 v[150:153], v[214:221], v[18:25], 0, v211, v210 op_sel_hi:[0,0,0]
	v_mfma_scale_f32_16x16x128_f8f6f4 v[146:149], v[222:229], v[18:25], 0, v211, v210 op_sel_hi:[0,0,0]
	ds_read_b128 v[18:21], v208 offset:16384
	ds_read_b128 v[22:25], v209 offset:16384
	v_mfma_scale_f32_16x16x128_f8f6f4 v[138:141], v[214:221], v[42:49], 0, v211, v210 op_sel_hi:[0,0,0]
	v_mfma_scale_f32_16x16x128_f8f6f4 v[134:137], v[222:229], v[42:49], 0, v211, v210 op_sel_hi:[0,0,0]
	ds_read_b128 v[42:45], v208 offset:22528
	ds_read_b128 v[46:49], v209 offset:22528
	v_mfma_scale_f32_16x16x128_f8f6f4 v[126:129], v[214:221], v[34:41], 0, v211, v210 op_sel_hi:[0,0,0]
	v_mfma_scale_f32_16x16x128_f8f6f4 v[122:125], v[222:229], v[34:41], 0, v211, v210 op_sel_hi:[0,0,0]
	ds_read_b128 v[34:37], v208 offset:20480
	ds_read_b128 v[38:41], v209 offset:20480
	s_setprio 0
	s_mov_b32 m0, s41
	s_barrier
	global_load_lds_dwordx4 v184, s[36:37]
	s_mov_b32 m0, s44
	v_mov_b32_e32 v191, v185
	global_load_lds_dwordx4 v190, s[36:37]
	s_barrier
	s_waitcnt lgkmcnt(0)
	v_lshl_add_u64 v[234:235], s[36:37], 0, v[184:185]
	v_lshl_add_u64 v[236:237], s[36:37], 0, v[190:191]
	s_setprio 1
	s_waitcnt lgkmcnt(0)
	v_mfma_scale_f32_16x16x128_f8f6f4 v[110:113], v[2:9], v[18:25], 0, v211, v210 op_sel_hi:[0,0,0]
	v_mfma_scale_f32_16x16x128_f8f6f4 v[102:105], v[10:17], v[18:25], 0, v211, v210 op_sel_hi:[0,0,0]
	v_mfma_scale_f32_16x16x128_f8f6f4 v[94:97], v[2:9], v[26:33], 0, v211, v210 op_sel_hi:[0,0,0]
	v_mfma_scale_f32_16x16x128_f8f6f4 v[86:89], v[10:17], v[26:33], 0, v211, v210 op_sel_hi:[0,0,0]
	v_mfma_scale_f32_16x16x128_f8f6f4 v[78:81], v[2:9], v[34:41], 0, v211, v210 op_sel_hi:[0,0,0]
	v_mfma_scale_f32_16x16x128_f8f6f4 v[70:73], v[10:17], v[34:41], 0, v211, v210 op_sel_hi:[0,0,0]
	v_mfma_scale_f32_16x16x128_f8f6f4 v[62:65], v[2:9], v[42:49], 0, v211, v210 op_sel_hi:[0,0,0]
	v_mfma_scale_f32_16x16x128_f8f6f4 v[54:57], v[10:17], v[42:49], 0, v211, v210 op_sel_hi:[0,0,0]
	s_setprio 0
	s_barrier
	s_add_u32 s34, s28, 0x40000
	s_addc_u32 s35, s29, 0
	s_mov_b32 m0, s59
	v_lshl_add_u64 v[2:3], s[34:35], 0, v[188:189]
	global_load_lds_dwordx4 v[2:3], off
	v_lshl_add_u64 v[2:3], s[34:35], 0, v[186:187]
	s_mov_b32 m0, s60
	s_nop 0
	global_load_lds_dwordx4 v[2:3], off
	s_waitcnt vmcnt(6)
	s_barrier
	s_setprio 1
	v_mfma_scale_f32_16x16x128_f8f6f4 v[106:109], v[214:221], v[18:25], 0, v211, v210 op_sel_hi:[0,0,0]
	v_mfma_scale_f32_16x16x128_f8f6f4 v[98:101], v[222:229], v[18:25], 0, v211, v210 op_sel_hi:[0,0,0]
	ds_read_b128 v[18:21], v208 offset:32768
	ds_read_b128 v[22:25], v209 offset:32768
	v_mfma_scale_f32_16x16x128_f8f6f4 v[90:93], v[214:221], v[26:33], 0, v211, v210 op_sel_hi:[0,0,0]
	v_mfma_scale_f32_16x16x128_f8f6f4 v[82:85], v[222:229], v[26:33], 0, v211, v210 op_sel_hi:[0,0,0]
	ds_read_b128 v[26:29], v208 offset:34816
	ds_read_b128 v[30:33], v209 offset:34816
	v_mfma_scale_f32_16x16x128_f8f6f4 v[74:77], v[214:221], v[34:41], 0, v211, v210 op_sel_hi:[0,0,0]
	v_mfma_scale_f32_16x16x128_f8f6f4 v[66:69], v[222:229], v[34:41], 0, v211, v210 op_sel_hi:[0,0,0]
	ds_read_b128 v[34:37], v208 offset:36864
	ds_read_b128 v[38:41], v209 offset:36864
	v_mfma_scale_f32_16x16x128_f8f6f4 v[58:61], v[214:221], v[42:49], 0, v211, v210 op_sel_hi:[0,0,0]
	v_mfma_scale_f32_16x16x128_f8f6f4 v[50:53], v[222:229], v[42:49], 0, v211, v210 op_sel_hi:[0,0,0]
	ds_read_b128 v[42:45], v208 offset:38912
	ds_read_b128 v[46:49], v209 offset:38912
	s_setprio 0
	v_add_u32_e32 v6, s61, v204
	v_add_u32_e32 v14, s61, v205
	s_barrier
	ds_read_b128 v[2:5], v6
	ds_read_b128 v[10:13], v6 offset:2048
	ds_read_b128 v[6:9], v14
	ds_read_b128 v[14:17], v14 offset:2048
	s_mov_b32 m0, s45
	v_lshl_add_u64 v[214:215], s[36:37], 0, v[192:193]
	global_load_lds_dwordx4 v[214:215], off
	v_lshl_add_u64 v[214:215], s[36:37], 0, v[194:195]
	s_mov_b32 m0, s46
	s_nop 0
	global_load_lds_dwordx4 v[214:215], off
	s_waitcnt lgkmcnt(8)
	s_barrier
	s_waitcnt lgkmcnt(0)
	s_setprio 1
	s_waitcnt lgkmcnt(0)
	v_mfma_scale_f32_16x16x128_f8f6f4 v[174:177], v[2:9], v[18:25], v[174:177], v211, v210 op_sel_hi:[0,0,0]
	v_mfma_scale_f32_16x16x128_f8f6f4 v[170:173], v[10:17], v[18:25], v[170:173], v211, v210 op_sel_hi:[0,0,0]
	v_mfma_scale_f32_16x16x128_f8f6f4 v[166:169], v[2:9], v[26:33], v[166:169], v211, v210 op_sel_hi:[0,0,0]
	v_mfma_scale_f32_16x16x128_f8f6f4 v[162:165], v[10:17], v[26:33], v[162:165], v211, v210 op_sel_hi:[0,0,0]
	v_mfma_scale_f32_16x16x128_f8f6f4 v[142:145], v[2:9], v[34:41], v[142:145], v211, v210 op_sel_hi:[0,0,0]
	v_mfma_scale_f32_16x16x128_f8f6f4 v[130:133], v[10:17], v[34:41], v[130:133], v211, v210 op_sel_hi:[0,0,0]
	v_mfma_scale_f32_16x16x128_f8f6f4 v[118:121], v[2:9], v[42:49], v[118:121], v211, v210 op_sel_hi:[0,0,0]
	v_mfma_scale_f32_16x16x128_f8f6f4 v[114:117], v[10:17], v[42:49], v[114:117], v211, v210 op_sel_hi:[0,0,0]
	s_setprio 0
	s_barrier
	s_mov_b32 m0, s63
	v_add_u32_e32 v191, s62, v204
	v_lshl_add_u64 v[230:231], v[230:231], 0, s[12:13]
	v_add_u32_e32 v193, s62, v205
	ds_read_b128 v[214:217], v191
	ds_read_b128 v[222:225], v191 offset:2048
	ds_read_b128 v[218:221], v193
	ds_read_b128 v[226:229], v193 offset:2048
	global_load_lds_dwordx4 v[230:231], off
	v_lshl_add_u64 v[230:231], v[232:233], 0, s[12:13]
	s_add_i32 m0, s63, 0x2000
	s_nop 0
	global_load_lds_dwordx4 v[230:231], off
	s_barrier
	s_waitcnt lgkmcnt(0)
	s_setprio 1
	s_waitcnt lgkmcnt(0)
	v_mfma_scale_f32_16x16x128_f8f6f4 v[158:161], v[214:221], v[18:25], v[158:161], v211, v210 op_sel_hi:[0,0,0]
	v_mfma_scale_f32_16x16x128_f8f6f4 v[154:157], v[222:229], v[18:25], v[154:157], v211, v210 op_sel_hi:[0,0,0]
	ds_read_b128 v[18:21], v208 offset:49152
	ds_read_b128 v[22:25], v209 offset:49152
	v_mfma_scale_f32_16x16x128_f8f6f4 v[150:153], v[214:221], v[26:33], v[150:153], v211, v210 op_sel_hi:[0,0,0]
	v_mfma_scale_f32_16x16x128_f8f6f4 v[146:149], v[222:229], v[26:33], v[146:149], v211, v210 op_sel_hi:[0,0,0]
	ds_read_b128 v[26:29], v208 offset:51200
	ds_read_b128 v[30:33], v209 offset:51200
	v_mfma_scale_f32_16x16x128_f8f6f4 v[138:141], v[214:221], v[34:41], v[138:141], v211, v210 op_sel_hi:[0,0,0]
	v_mfma_scale_f32_16x16x128_f8f6f4 v[134:137], v[222:229], v[34:41], v[134:137], v211, v210 op_sel_hi:[0,0,0]
	ds_read_b128 v[34:37], v208 offset:53248
	ds_read_b128 v[38:41], v209 offset:53248
	v_mfma_scale_f32_16x16x128_f8f6f4 v[126:129], v[214:221], v[42:49], v[126:129], v211, v210 op_sel_hi:[0,0,0]
	v_mfma_scale_f32_16x16x128_f8f6f4 v[122:125], v[222:229], v[42:49], v[122:125], v211, v210 op_sel_hi:[0,0,0]
	ds_read_b128 v[42:45], v208 offset:55296
	ds_read_b128 v[46:49], v209 offset:55296
	s_setprio 0
	s_mov_b32 m0, s49
	v_lshl_add_u64 v[230:231], v[234:235], 0, s[12:13]
	s_barrier
	global_load_lds_dwordx4 v[230:231], off
	v_lshl_add_u64 v[230:231], v[236:237], 0, s[12:13]
	s_mov_b32 m0, s50
	s_nop 0
	global_load_lds_dwordx4 v[230:231], off
	s_barrier
	s_waitcnt lgkmcnt(0)
	s_setprio 1
	s_waitcnt lgkmcnt(0)
	v_mfma_scale_f32_16x16x128_f8f6f4 v[110:113], v[2:9], v[18:25], v[110:113], v211, v210 op_sel_hi:[0,0,0]
	v_mfma_scale_f32_16x16x128_f8f6f4 v[102:105], v[10:17], v[18:25], v[102:105], v211, v210 op_sel_hi:[0,0,0]
	v_mfma_scale_f32_16x16x128_f8f6f4 v[94:97], v[2:9], v[26:33], v[94:97], v211, v210 op_sel_hi:[0,0,0]
	v_mfma_scale_f32_16x16x128_f8f6f4 v[86:89], v[10:17], v[26:33], v[86:89], v211, v210 op_sel_hi:[0,0,0]
	v_mfma_scale_f32_16x16x128_f8f6f4 v[78:81], v[2:9], v[34:41], v[78:81], v211, v210 op_sel_hi:[0,0,0]
	v_mfma_scale_f32_16x16x128_f8f6f4 v[70:73], v[10:17], v[34:41], v[70:73], v211, v210 op_sel_hi:[0,0,0]
	v_mfma_scale_f32_16x16x128_f8f6f4 v[62:65], v[2:9], v[42:49], v[62:65], v211, v210 op_sel_hi:[0,0,0]
	v_mfma_scale_f32_16x16x128_f8f6f4 v[54:57], v[10:17], v[42:49], v[54:57], v211, v210 op_sel_hi:[0,0,0]
	s_setprio 0
	s_barrier
	s_add_u32 s28, s28, 0x40080
	s_addc_u32 s29, s29, 0
	s_add_i32 s34, s62, s40
	v_lshl_add_u64 v[2:3], s[28:29], 0, v[188:189]
	s_mov_b32 m0, s34
	s_nop 0
	global_load_lds_dwordx4 v[2:3], off
	v_lshl_add_u64 v[2:3], s[28:29], 0, v[186:187]
	s_add_i32 m0, s34, 0x2000
	s_nop 0
	global_load_lds_dwordx4 v[2:3], off
	s_waitcnt vmcnt(6)
	s_barrier
	s_setprio 1
	v_mfma_scale_f32_16x16x128_f8f6f4 v[106:109], v[214:221], v[18:25], v[106:109], v211, v210 op_sel_hi:[0,0,0]
	v_mfma_scale_f32_16x16x128_f8f6f4 v[98:101], v[222:229], v[18:25], v[98:101], v211, v210 op_sel_hi:[0,0,0]
	v_mfma_scale_f32_16x16x128_f8f6f4 v[90:93], v[214:221], v[26:33], v[90:93], v211, v210 op_sel_hi:[0,0,0]
	v_mfma_scale_f32_16x16x128_f8f6f4 v[82:85], v[222:229], v[26:33], v[82:85], v211, v210 op_sel_hi:[0,0,0]
	v_mfma_scale_f32_16x16x128_f8f6f4 v[74:77], v[214:221], v[34:41], v[74:77], v211, v210 op_sel_hi:[0,0,0]
	v_mfma_scale_f32_16x16x128_f8f6f4 v[66:69], v[222:229], v[34:41], v[66:69], v211, v210 op_sel_hi:[0,0,0]
	v_mfma_scale_f32_16x16x128_f8f6f4 v[58:61], v[214:221], v[42:49], v[58:61], v211, v210 op_sel_hi:[0,0,0]
	v_mfma_scale_f32_16x16x128_f8f6f4 v[50:53], v[222:229], v[42:49], v[50:53], v211, v210 op_sel_hi:[0,0,0]
	s_setprio 0
	s_cmp_ge_i32 s71, s39
	s_barrier
	s_cbranch_scc1 .LBB0_1546
	s_mov_b64 s[28:29], s[30:31]
	s_branch .LBB0_1551

.LBB0_1553:
	s_add_i32 s71, s71, 2
	s_add_u32 s30, s28, 0x100
	s_addc_u32 s31, s29, 0
	s_and_b64 s[36:37], s[34:35], exec
	s_cselect_b32 s36, 0, s30
	s_cselect_b32 s37, 0, s31
	s_add_u32 s36, s22, s36
	s_addc_u32 s37, s23, s37
	s_add_u32 s72, s69, s28
	s_addc_u32 s73, s70, s29
	s_and_b64 s[28:29], s[34:35], exec
	s_cselect_b32 s29, s67, s73
	s_cselect_b32 s28, s68, s72
	s_mov_b32 m0, s42
	v_add_u32_e32 v191, s57, v204
	v_lshl_add_u64 v[230:231], s[28:29], 0, v[188:189]
	v_add_u32_e32 v197, s57, v205
	ds_read_b128 v[214:217], v191
	ds_read_b128 v[222:225], v191 offset:2048
	ds_read_b128 v[218:221], v197
	ds_read_b128 v[226:229], v197 offset:2048
	global_load_lds_dwordx4 v[230:231], off
	v_lshl_add_u64 v[232:233], s[28:29], 0, v[186:187]
	s_mov_b32 m0, s43
	s_waitcnt lgkmcnt(0)
	v_mfma_scale_f32_16x16x128_f8f6f4 v[174:177], v[2:9], v[26:33], v[174:177], v211, v210 op_sel_hi:[0,0,0]
	global_load_lds_dwordx4 v[232:233], off
	s_barrier
	s_waitcnt lgkmcnt(0)
	v_mov_b32_e32 v193, v185
	v_mov_b32_e32 v195, v185
	v_mfma_scale_f32_16x16x128_f8f6f4 v[170:173], v[10:17], v[26:33], v[170:173], v211, v210 op_sel_hi:[0,0,0]
	v_mfma_scale_f32_16x16x128_f8f6f4 v[166:169], v[2:9], v[18:25], v[166:169], v211, v210 op_sel_hi:[0,0,0]
	v_mfma_scale_f32_16x16x128_f8f6f4 v[162:165], v[10:17], v[18:25], v[162:165], v211, v210 op_sel_hi:[0,0,0]
	v_mfma_scale_f32_16x16x128_f8f6f4 v[142:145], v[2:9], v[42:49], v[142:145], v211, v210 op_sel_hi:[0,0,0]
	v_mfma_scale_f32_16x16x128_f8f6f4 v[130:133], v[10:17], v[42:49], v[130:133], v211, v210 op_sel_hi:[0,0,0]
	v_mfma_scale_f32_16x16x128_f8f6f4 v[118:121], v[2:9], v[34:41], v[118:121], v211, v210 op_sel_hi:[0,0,0]
	v_mfma_scale_f32_16x16x128_f8f6f4 v[114:117], v[10:17], v[34:41], v[114:117], v211, v210 op_sel_hi:[0,0,0]
	s_setprio 1
	v_mfma_scale_f32_16x16x128_f8f6f4 v[158:161], v[214:221], v[26:33], v[158:161], v211, v210 op_sel_hi:[0,0,0]
	v_mfma_scale_f32_16x16x128_f8f6f4 v[154:157], v[222:229], v[26:33], v[154:157], v211, v210 op_sel_hi:[0,0,0]
	ds_read_b128 v[26:29], v208 offset:18432
	ds_read_b128 v[30:33], v209 offset:18432
	v_mfma_scale_f32_16x16x128_f8f6f4 v[150:153], v[214:221], v[18:25], v[150:153], v211, v210 op_sel_hi:[0,0,0]
	v_mfma_scale_f32_16x16x128_f8f6f4 v[146:149], v[222:229], v[18:25], v[146:149], v211, v210 op_sel_hi:[0,0,0]
	ds_read_b128 v[18:21], v208 offset:16384
	ds_read_b128 v[22:25], v209 offset:16384
	v_mfma_scale_f32_16x16x128_f8f6f4 v[138:141], v[214:221], v[42:49], v[138:141], v211, v210 op_sel_hi:[0,0,0]
	v_mfma_scale_f32_16x16x128_f8f6f4 v[134:137], v[222:229], v[42:49], v[134:137], v211, v210 op_sel_hi:[0,0,0]
	ds_read_b128 v[42:45], v208 offset:22528
	ds_read_b128 v[46:49], v209 offset:22528
	v_mfma_scale_f32_16x16x128_f8f6f4 v[126:129], v[214:221], v[34:41], v[126:129], v211, v210 op_sel_hi:[0,0,0]
	v_mfma_scale_f32_16x16x128_f8f6f4 v[122:125], v[222:229], v[34:41], v[122:125], v211, v210 op_sel_hi:[0,0,0]
	ds_read_b128 v[34:37], v208 offset:20480
	ds_read_b128 v[38:41], v209 offset:20480
	s_setprio 0
	s_mov_b32 m0, s41
	s_barrier
	global_load_lds_dwordx4 v184, s[36:37]
	s_mov_b32 m0, s44
	v_mov_b32_e32 v191, v185
	global_load_lds_dwordx4 v190, s[36:37]
	s_barrier
	s_waitcnt lgkmcnt(0)
	v_lshl_add_u64 v[234:235], s[36:37], 0, v[184:185]
	v_lshl_add_u64 v[236:237], s[36:37], 0, v[190:191]
	s_setprio 1
	s_waitcnt lgkmcnt(0)
	v_mfma_scale_f32_16x16x128_f8f6f4 v[110:113], v[2:9], v[18:25], v[110:113], v211, v210 op_sel_hi:[0,0,0]
	v_mfma_scale_f32_16x16x128_f8f6f4 v[102:105], v[10:17], v[18:25], v[102:105], v211, v210 op_sel_hi:[0,0,0]
	v_mfma_scale_f32_16x16x128_f8f6f4 v[94:97], v[2:9], v[26:33], v[94:97], v211, v210 op_sel_hi:[0,0,0]
	v_mfma_scale_f32_16x16x128_f8f6f4 v[86:89], v[10:17], v[26:33], v[86:89], v211, v210 op_sel_hi:[0,0,0]
	v_mfma_scale_f32_16x16x128_f8f6f4 v[78:81], v[2:9], v[34:41], v[78:81], v211, v210 op_sel_hi:[0,0,0]
	v_mfma_scale_f32_16x16x128_f8f6f4 v[70:73], v[10:17], v[34:41], v[70:73], v211, v210 op_sel_hi:[0,0,0]
	v_mfma_scale_f32_16x16x128_f8f6f4 v[62:65], v[2:9], v[42:49], v[62:65], v211, v210 op_sel_hi:[0,0,0]
	v_mfma_scale_f32_16x16x128_f8f6f4 v[54:57], v[10:17], v[42:49], v[54:57], v211, v210 op_sel_hi:[0,0,0]
	s_setprio 0
	s_barrier
	s_add_u32 s34, s28, 0x40000
	s_addc_u32 s35, s29, 0
	s_mov_b32 m0, s59
	v_lshl_add_u64 v[2:3], s[34:35], 0, v[188:189]
	global_load_lds_dwordx4 v[2:3], off
	v_lshl_add_u64 v[2:3], s[34:35], 0, v[186:187]
	s_mov_b32 m0, s60
	s_nop 0
	global_load_lds_dwordx4 v[2:3], off
	s_waitcnt vmcnt(6)
	s_barrier
	s_setprio 1
	v_mfma_scale_f32_16x16x128_f8f6f4 v[106:109], v[214:221], v[18:25], v[106:109], v211, v210 op_sel_hi:[0,0,0]
	v_mfma_scale_f32_16x16x128_f8f6f4 v[98:101], v[222:229], v[18:25], v[98:101], v211, v210 op_sel_hi:[0,0,0]
	ds_read_b128 v[18:21], v208 offset:32768
	ds_read_b128 v[22:25], v209 offset:32768
	v_mfma_scale_f32_16x16x128_f8f6f4 v[90:93], v[214:221], v[26:33], v[90:93], v211, v210 op_sel_hi:[0,0,0]
	v_mfma_scale_f32_16x16x128_f8f6f4 v[82:85], v[222:229], v[26:33], v[82:85], v211, v210 op_sel_hi:[0,0,0]
	ds_read_b128 v[26:29], v208 offset:34816
	ds_read_b128 v[30:33], v209 offset:34816
	v_mfma_scale_f32_16x16x128_f8f6f4 v[74:77], v[214:221], v[34:41], v[74:77], v211, v210 op_sel_hi:[0,0,0]
	v_mfma_scale_f32_16x16x128_f8f6f4 v[66:69], v[222:229], v[34:41], v[66:69], v211, v210 op_sel_hi:[0,0,0]
	ds_read_b128 v[34:37], v208 offset:36864
	ds_read_b128 v[38:41], v209 offset:36864
	v_mfma_scale_f32_16x16x128_f8f6f4 v[58:61], v[214:221], v[42:49], v[58:61], v211, v210 op_sel_hi:[0,0,0]
	v_mfma_scale_f32_16x16x128_f8f6f4 v[50:53], v[222:229], v[42:49], v[50:53], v211, v210 op_sel_hi:[0,0,0]
	ds_read_b128 v[42:45], v208 offset:38912
	ds_read_b128 v[46:49], v209 offset:38912
	s_setprio 0
	v_add_u32_e32 v6, s61, v204
	v_add_u32_e32 v14, s61, v205
	s_barrier
	ds_read_b128 v[2:5], v6
	ds_read_b128 v[10:13], v6 offset:2048
	ds_read_b128 v[6:9], v14
	ds_read_b128 v[14:17], v14 offset:2048
	s_mov_b32 m0, s45
	v_lshl_add_u64 v[214:215], s[36:37], 0, v[192:193]
	global_load_lds_dwordx4 v[214:215], off
	v_lshl_add_u64 v[214:215], s[36:37], 0, v[194:195]
	s_mov_b32 m0, s46
	s_nop 0
	global_load_lds_dwordx4 v[214:215], off
	s_waitcnt lgkmcnt(8)
	s_barrier
	s_waitcnt lgkmcnt(0)
	s_setprio 1
	s_waitcnt lgkmcnt(0)
	v_mfma_scale_f32_16x16x128_f8f6f4 v[174:177], v[2:9], v[18:25], v[174:177], v211, v210 op_sel_hi:[0,0,0]
	v_mfma_scale_f32_16x16x128_f8f6f4 v[170:173], v[10:17], v[18:25], v[170:173], v211, v210 op_sel_hi:[0,0,0]
	v_mfma_scale_f32_16x16x128_f8f6f4 v[166:169], v[2:9], v[26:33], v[166:169], v211, v210 op_sel_hi:[0,0,0]
	v_mfma_scale_f32_16x16x128_f8f6f4 v[162:165], v[10:17], v[26:33], v[162:165], v211, v210 op_sel_hi:[0,0,0]
	v_mfma_scale_f32_16x16x128_f8f6f4 v[142:145], v[2:9], v[34:41], v[142:145], v211, v210 op_sel_hi:[0,0,0]
	v_mfma_scale_f32_16x16x128_f8f6f4 v[130:133], v[10:17], v[34:41], v[130:133], v211, v210 op_sel_hi:[0,0,0]
	v_mfma_scale_f32_16x16x128_f8f6f4 v[118:121], v[2:9], v[42:49], v[118:121], v211, v210 op_sel_hi:[0,0,0]
	v_mfma_scale_f32_16x16x128_f8f6f4 v[114:117], v[10:17], v[42:49], v[114:117], v211, v210 op_sel_hi:[0,0,0]
	s_setprio 0
	s_barrier
	s_mov_b32 m0, s63
	v_add_u32_e32 v191, s62, v204
	v_lshl_add_u64 v[230:231], v[230:231], 0, s[12:13]
	v_add_u32_e32 v193, s62, v205
	ds_read_b128 v[214:217], v191
	ds_read_b128 v[222:225], v191 offset:2048
	ds_read_b128 v[218:221], v193
	ds_read_b128 v[226:229], v193 offset:2048
	global_load_lds_dwordx4 v[230:231], off
	v_lshl_add_u64 v[230:231], v[232:233], 0, s[12:13]
	s_add_i32 m0, s63, 0x2000
	s_nop 0
	global_load_lds_dwordx4 v[230:231], off
	s_barrier
	s_waitcnt lgkmcnt(0)
	s_setprio 1
	s_waitcnt lgkmcnt(0)
	v_mfma_scale_f32_16x16x128_f8f6f4 v[158:161], v[214:221], v[18:25], v[158:161], v211, v210 op_sel_hi:[0,0,0]
	v_mfma_scale_f32_16x16x128_f8f6f4 v[154:157], v[222:229], v[18:25], v[154:157], v211, v210 op_sel_hi:[0,0,0]
	ds_read_b128 v[18:21], v208 offset:49152
	ds_read_b128 v[22:25], v209 offset:49152
	v_mfma_scale_f32_16x16x128_f8f6f4 v[150:153], v[214:221], v[26:33], v[150:153], v211, v210 op_sel_hi:[0,0,0]
	v_mfma_scale_f32_16x16x128_f8f6f4 v[146:149], v[222:229], v[26:33], v[146:149], v211, v210 op_sel_hi:[0,0,0]
	ds_read_b128 v[26:29], v208 offset:51200
	ds_read_b128 v[30:33], v209 offset:51200
	v_mfma_scale_f32_16x16x128_f8f6f4 v[138:141], v[214:221], v[34:41], v[138:141], v211, v210 op_sel_hi:[0,0,0]
	v_mfma_scale_f32_16x16x128_f8f6f4 v[134:137], v[222:229], v[34:41], v[134:137], v211, v210 op_sel_hi:[0,0,0]
	ds_read_b128 v[34:37], v208 offset:53248
	ds_read_b128 v[38:41], v209 offset:53248
	v_mfma_scale_f32_16x16x128_f8f6f4 v[126:129], v[214:221], v[42:49], v[126:129], v211, v210 op_sel_hi:[0,0,0]
	v_mfma_scale_f32_16x16x128_f8f6f4 v[122:125], v[222:229], v[42:49], v[122:125], v211, v210 op_sel_hi:[0,0,0]
	ds_read_b128 v[42:45], v208 offset:55296
	ds_read_b128 v[46:49], v209 offset:55296
	s_setprio 0
	s_mov_b32 m0, s49
	v_lshl_add_u64 v[230:231], v[234:235], 0, s[12:13]
	s_barrier
	global_load_lds_dwordx4 v[230:231], off
	v_lshl_add_u64 v[230:231], v[236:237], 0, s[12:13]
	s_mov_b32 m0, s50
	s_nop 0
	global_load_lds_dwordx4 v[230:231], off
	s_barrier
	s_waitcnt lgkmcnt(0)
	s_setprio 1
	s_waitcnt lgkmcnt(0)
	v_mfma_scale_f32_16x16x128_f8f6f4 v[110:113], v[2:9], v[18:25], v[110:113], v211, v210 op_sel_hi:[0,0,0]
	v_mfma_scale_f32_16x16x128_f8f6f4 v[102:105], v[10:17], v[18:25], v[102:105], v211, v210 op_sel_hi:[0,0,0]
	v_mfma_scale_f32_16x16x128_f8f6f4 v[94:97], v[2:9], v[26:33], v[94:97], v211, v210 op_sel_hi:[0,0,0]
	v_mfma_scale_f32_16x16x128_f8f6f4 v[86:89], v[10:17], v[26:33], v[86:89], v211, v210 op_sel_hi:[0,0,0]
	v_mfma_scale_f32_16x16x128_f8f6f4 v[78:81], v[2:9], v[34:41], v[78:81], v211, v210 op_sel_hi:[0,0,0]
	v_mfma_scale_f32_16x16x128_f8f6f4 v[70:73], v[10:17], v[34:41], v[70:73], v211, v210 op_sel_hi:[0,0,0]
	v_mfma_scale_f32_16x16x128_f8f6f4 v[62:65], v[2:9], v[42:49], v[62:65], v211, v210 op_sel_hi:[0,0,0]
	v_mfma_scale_f32_16x16x128_f8f6f4 v[54:57], v[10:17], v[42:49], v[54:57], v211, v210 op_sel_hi:[0,0,0]
	s_setprio 0
	s_barrier
	s_add_u32 s28, s28, 0x40080
	s_addc_u32 s29, s29, 0
	s_add_i32 s34, s62, s40
	v_lshl_add_u64 v[2:3], s[28:29], 0, v[188:189]
	s_mov_b32 m0, s34
	s_nop 0
	global_load_lds_dwordx4 v[2:3], off
	v_lshl_add_u64 v[2:3], s[28:29], 0, v[186:187]
	s_add_i32 m0, s34, 0x2000
	s_nop 0
	global_load_lds_dwordx4 v[2:3], off
	s_waitcnt vmcnt(6)
	s_barrier
	s_setprio 1
	v_mfma_scale_f32_16x16x128_f8f6f4 v[106:109], v[214:221], v[18:25], v[106:109], v211, v210 op_sel_hi:[0,0,0]
	v_mfma_scale_f32_16x16x128_f8f6f4 v[98:101], v[222:229], v[18:25], v[98:101], v211, v210 op_sel_hi:[0,0,0]
	v_mfma_scale_f32_16x16x128_f8f6f4 v[90:93], v[214:221], v[26:33], v[90:93], v211, v210 op_sel_hi:[0,0,0]
	v_mfma_scale_f32_16x16x128_f8f6f4 v[82:85], v[222:229], v[26:33], v[82:85], v211, v210 op_sel_hi:[0,0,0]
	v_mfma_scale_f32_16x16x128_f8f6f4 v[74:77], v[214:221], v[34:41], v[74:77], v211, v210 op_sel_hi:[0,0,0]
	v_mfma_scale_f32_16x16x128_f8f6f4 v[66:69], v[222:229], v[34:41], v[66:69], v211, v210 op_sel_hi:[0,0,0]
	v_mfma_scale_f32_16x16x128_f8f6f4 v[58:61], v[214:221], v[42:49], v[58:61], v211, v210 op_sel_hi:[0,0,0]
	v_mfma_scale_f32_16x16x128_f8f6f4 v[50:53], v[222:229], v[42:49], v[50:53], v211, v210 op_sel_hi:[0,0,0]
	s_setprio 0
	s_cmp_ge_i32 s71, s39
	s_barrier
	s_cbranch_scc1 .LBB0_1546
	s_mov_b64 s[28:29], s[30:31]
	s_branch .LBB0_1551

.Lmy_pl3_1675:
	s_add_i32 s59, s59, 2
	s_add_u32 s24, s22, 0x100
	s_addc_u32 s25, s23, 0
	s_and_b64 s[28:29], s[26:27], exec
	s_cselect_b32 s28, 0, s24
	s_cselect_b32 s29, 0, s25
	s_add_u32 s28, s12, s28
	s_addc_u32 s29, s13, s29
	s_add_u32 s60, s57, s22
	s_addc_u32 s61, s58, s23
	s_and_b64 s[22:23], s[26:27], exec
	s_cselect_b32 s23, s55, s61
	s_cselect_b32 s22, s56, s60
	s_mov_b32 m0, s5
	s_waitcnt lgkmcnt(0)
	v_mfma_scale_f32_16x16x128_f8f6f4 v[222:225], v[2:9], v[42:49], 0, v209, v208 op_sel_hi:[0,0,0]
	v_lshl_add_u64 v[238:239], s[22:23], 0, v[188:189]
	v_add_u32_e32 v191, s46, v203
	v_lshl_add_u64 v[240:241], s[22:23], 0, v[186:187]
	v_mov_b32_e32 v193, v185
	v_mov_b32_e32 v195, v185
	s_nop 1
	v_add_u32_e32 v142, s46, v202
	v_mfma_scale_f32_16x16x128_f8f6f4 v[226:229], v[10:17], v[42:49], 0, v209, v208 op_sel_hi:[0,0,0]
	s_nop 6
	ds_read_b128 v[138:141], v142
	ds_read_b128 v[214:217], v142 offset:2048
	ds_read_b128 v[142:145], v191
	ds_read_b128 v[218:221], v191 offset:2048
	global_load_lds_dwordx4 v[238:239], off
	s_mov_b32 m0, s31
	s_nop 0
	global_load_lds_dwordx4 v[240:241], off
	v_mfma_scale_f32_16x16x128_f8f6f4 v[174:177], v[2:9], v[26:33], 0, v209, v208 op_sel_hi:[0,0,0]
	s_barrier
	s_waitcnt lgkmcnt(0)
	v_mfma_scale_f32_16x16x128_f8f6f4 v[170:173], v[10:17], v[26:33], 0, v209, v208 op_sel_hi:[0,0,0]
	v_mfma_scale_f32_16x16x128_f8f6f4 v[166:169], v[2:9], v[18:25], 0, v209, v208 op_sel_hi:[0,0,0]
	v_mfma_scale_f32_16x16x128_f8f6f4 v[162:165], v[10:17], v[18:25], 0, v209, v208 op_sel_hi:[0,0,0]
	v_mfma_scale_f32_16x16x128_f8f6f4 v[134:137], v[2:9], v[34:41], 0, v209, v208 op_sel_hi:[0,0,0]
	v_mfma_scale_f32_16x16x128_f8f6f4 v[122:125], v[10:17], v[34:41], 0, v209, v208 op_sel_hi:[0,0,0]
	s_setprio 1
	s_waitcnt lgkmcnt(0)
	v_mfma_scale_f32_16x16x128_f8f6f4 v[158:161], v[138:145], v[26:33], 0, v209, v208 op_sel_hi:[0,0,0]
	v_mfma_scale_f32_16x16x128_f8f6f4 v[154:157], v[214:221], v[26:33], 0, v209, v208 op_sel_hi:[0,0,0]
	ds_read_b128 v[26:29], v206 offset:18432
	ds_read_b128 v[30:33], v207 offset:18432
	v_mfma_scale_f32_16x16x128_f8f6f4 v[150:153], v[138:145], v[18:25], 0, v209, v208 op_sel_hi:[0,0,0]
	v_mfma_scale_f32_16x16x128_f8f6f4 v[146:149], v[214:221], v[18:25], 0, v209, v208 op_sel_hi:[0,0,0]
	ds_read_b128 v[18:21], v206 offset:16384
	ds_read_b128 v[22:25], v207 offset:16384
	v_mfma_scale_f32_16x16x128_f8f6f4 v[130:133], v[138:145], v[42:49], 0, v209, v208 op_sel_hi:[0,0,0]
	v_mfma_scale_f32_16x16x128_f8f6f4 v[126:129], v[214:221], v[42:49], 0, v209, v208 op_sel_hi:[0,0,0]
	ds_read_b128 v[42:45], v206 offset:22528
	ds_read_b128 v[46:49], v207 offset:22528
	v_mfma_scale_f32_16x16x128_f8f6f4 v[118:121], v[138:145], v[34:41], 0, v209, v208 op_sel_hi:[0,0,0]
	v_mfma_scale_f32_16x16x128_f8f6f4 v[114:117], v[214:221], v[34:41], 0, v209, v208 op_sel_hi:[0,0,0]
	ds_read_b128 v[34:37], v206 offset:20480
	ds_read_b128 v[38:41], v207 offset:20480
	s_setprio 0
	s_mov_b32 m0, s4
	s_barrier
	global_load_lds_dwordx4 v184, s[28:29]
	s_mov_b32 m0, s33
	v_mov_b32_e32 v191, v185
	global_load_lds_dwordx4 v190, s[28:29]
	s_barrier
	s_waitcnt lgkmcnt(0)
	v_lshl_add_u64 v[242:243], s[28:29], 0, v[184:185]
	v_lshl_add_u64 v[244:245], s[28:29], 0, v[190:191]
	s_setprio 1
	s_waitcnt lgkmcnt(0)
	v_mfma_scale_f32_16x16x128_f8f6f4 v[110:113], v[2:9], v[18:25], 0, v209, v208 op_sel_hi:[0,0,0]
	v_mfma_scale_f32_16x16x128_f8f6f4 v[106:109], v[10:17], v[18:25], 0, v209, v208 op_sel_hi:[0,0,0]
	v_mfma_scale_f32_16x16x128_f8f6f4 v[102:105], v[2:9], v[26:33], 0, v209, v208 op_sel_hi:[0,0,0]
	v_mfma_scale_f32_16x16x128_f8f6f4 v[98:101], v[10:17], v[26:33], 0, v209, v208 op_sel_hi:[0,0,0]
	v_mfma_scale_f32_16x16x128_f8f6f4 v[78:81], v[2:9], v[34:41], 0, v209, v208 op_sel_hi:[0,0,0]
	v_mfma_scale_f32_16x16x128_f8f6f4 v[74:77], v[10:17], v[34:41], 0, v209, v208 op_sel_hi:[0,0,0]
	v_mfma_scale_f32_16x16x128_f8f6f4 v[70:73], v[2:9], v[42:49], 0, v209, v208 op_sel_hi:[0,0,0]
	v_mfma_scale_f32_16x16x128_f8f6f4 v[66:69], v[10:17], v[42:49], 0, v209, v208 op_sel_hi:[0,0,0]
	s_setprio 0
	s_barrier
	s_add_u32 s26, s22, 0x10000
	s_addc_u32 s27, s23, 0
	s_mov_b32 m0, s48
	v_lshl_add_u64 v[2:3], s[26:27], 0, v[188:189]
	global_load_lds_dwordx4 v[2:3], off
	v_lshl_add_u64 v[2:3], s[26:27], 0, v[186:187]
	s_mov_b32 m0, s49
	s_nop 0
	global_load_lds_dwordx4 v[2:3], off
	s_waitcnt vmcnt(6)
	s_barrier
	s_setprio 1
	v_mfma_scale_f32_16x16x128_f8f6f4 v[94:97], v[138:145], v[18:25], 0, v209, v208 op_sel_hi:[0,0,0]
	v_mfma_scale_f32_16x16x128_f8f6f4 v[90:93], v[214:221], v[18:25], 0, v209, v208 op_sel_hi:[0,0,0]
	ds_read_b128 v[18:21], v206 offset:32768
	ds_read_b128 v[22:25], v207 offset:32768
	v_mfma_scale_f32_16x16x128_f8f6f4 v[86:89], v[138:145], v[26:33], 0, v209, v208 op_sel_hi:[0,0,0]
	v_mfma_scale_f32_16x16x128_f8f6f4 v[82:85], v[214:221], v[26:33], 0, v209, v208 op_sel_hi:[0,0,0]
	ds_read_b128 v[26:29], v206 offset:34816
	ds_read_b128 v[30:33], v207 offset:34816
	v_mfma_scale_f32_16x16x128_f8f6f4 v[62:65], v[138:145], v[34:41], 0, v209, v208 op_sel_hi:[0,0,0]
	v_mfma_scale_f32_16x16x128_f8f6f4 v[58:61], v[214:221], v[34:41], 0, v209, v208 op_sel_hi:[0,0,0]
	ds_read_b128 v[34:37], v206 offset:36864
	ds_read_b128 v[38:41], v207 offset:36864
	v_mfma_scale_f32_16x16x128_f8f6f4 v[230:233], v[138:145], v[42:49], 0, v209, v208 op_sel_hi:[0,0,0]
	v_mfma_scale_f32_16x16x128_f8f6f4 v[234:237], v[214:221], v[42:49], 0, v209, v208 op_sel_hi:[0,0,0]
	ds_read_b128 v[42:45], v206 offset:38912
	ds_read_b128 v[46:49], v207 offset:38912
	s_setprio 0
	v_add_u32_e32 v6, s50, v202
	v_add_u32_e32 v14, s50, v203
	s_barrier
	ds_read_b128 v[2:5], v6
	ds_read_b128 v[10:13], v6 offset:2048
	ds_read_b128 v[6:9], v14
	ds_read_b128 v[14:17], v14 offset:2048
	s_mov_b32 m0, s34
	v_lshl_add_u64 v[50:51], s[28:29], 0, v[192:193]
	global_load_lds_dwordx4 v[50:51], off
	v_lshl_add_u64 v[50:51], s[28:29], 0, v[194:195]
	s_mov_b32 m0, s35
	s_nop 0
	global_load_lds_dwordx4 v[50:51], off
	s_waitcnt lgkmcnt(8)
	s_barrier
	s_waitcnt lgkmcnt(0)
	s_setprio 1
	s_waitcnt lgkmcnt(0)
	v_mfma_scale_f32_16x16x128_f8f6f4 v[174:177], v[2:9], v[18:25], v[174:177], v209, v208 op_sel_hi:[0,0,0]
	v_mfma_scale_f32_16x16x128_f8f6f4 v[170:173], v[10:17], v[18:25], v[170:173], v209, v208 op_sel_hi:[0,0,0]
	v_mfma_scale_f32_16x16x128_f8f6f4 v[166:169], v[2:9], v[26:33], v[166:169], v209, v208 op_sel_hi:[0,0,0]
	v_mfma_scale_f32_16x16x128_f8f6f4 v[162:165], v[10:17], v[26:33], v[162:165], v209, v208 op_sel_hi:[0,0,0]
	v_mfma_scale_f32_16x16x128_f8f6f4 v[142:145], v[2:9], v[34:41], v[222:225], v209, v208 op_sel_hi:[0,0,0]
	v_mfma_scale_f32_16x16x128_f8f6f4 v[138:141], v[10:17], v[34:41], v[226:229], v209, v208 op_sel_hi:[0,0,0]
	v_mfma_scale_f32_16x16x128_f8f6f4 v[134:137], v[2:9], v[42:49], v[134:137], v209, v208 op_sel_hi:[0,0,0]
	v_mfma_scale_f32_16x16x128_f8f6f4 v[122:125], v[10:17], v[42:49], v[122:125], v209, v208 op_sel_hi:[0,0,0]
	s_setprio 0
	s_barrier
	s_mov_b32 m0, s52
	v_add_u32_e32 v54, s51, v202
	v_lshl_add_u64 v[222:223], v[238:239], 0, s[8:9]
	v_add_u32_e32 v191, s51, v203
	ds_read_b128 v[50:53], v54
	ds_read_b128 v[214:217], v54 offset:2048
	ds_read_b128 v[54:57], v191
	ds_read_b128 v[218:221], v191 offset:2048
	global_load_lds_dwordx4 v[222:223], off
	v_lshl_add_u64 v[222:223], v[240:241], 0, s[8:9]
	s_mov_b32 m0, s53
	s_nop 0
	global_load_lds_dwordx4 v[222:223], off
	s_barrier
	s_waitcnt lgkmcnt(0)
	s_setprio 1
	s_waitcnt lgkmcnt(0)
	v_mfma_scale_f32_16x16x128_f8f6f4 v[158:161], v[50:57], v[18:25], v[158:161], v209, v208 op_sel_hi:[0,0,0]
	v_mfma_scale_f32_16x16x128_f8f6f4 v[154:157], v[214:221], v[18:25], v[154:157], v209, v208 op_sel_hi:[0,0,0]
	ds_read_b128 v[18:21], v206 offset:49152
	ds_read_b128 v[22:25], v207 offset:49152
	v_mfma_scale_f32_16x16x128_f8f6f4 v[150:153], v[50:57], v[26:33], v[150:153], v209, v208 op_sel_hi:[0,0,0]
	v_mfma_scale_f32_16x16x128_f8f6f4 v[146:149], v[214:221], v[26:33], v[146:149], v209, v208 op_sel_hi:[0,0,0]
	ds_read_b128 v[26:29], v206 offset:51200
	ds_read_b128 v[30:33], v207 offset:51200
	v_mfma_scale_f32_16x16x128_f8f6f4 v[130:133], v[50:57], v[34:41], v[130:133], v209, v208 op_sel_hi:[0,0,0]
	v_mfma_scale_f32_16x16x128_f8f6f4 v[126:129], v[214:221], v[34:41], v[126:129], v209, v208 op_sel_hi:[0,0,0]
	ds_read_b128 v[34:37], v206 offset:53248
	ds_read_b128 v[38:41], v207 offset:53248
	v_mfma_scale_f32_16x16x128_f8f6f4 v[118:121], v[50:57], v[42:49], v[118:121], v209, v208 op_sel_hi:[0,0,0]
	v_mfma_scale_f32_16x16x128_f8f6f4 v[114:117], v[214:221], v[42:49], v[114:117], v209, v208 op_sel_hi:[0,0,0]
	ds_read_b128 v[42:45], v206 offset:55296
	ds_read_b128 v[46:49], v207 offset:55296
	s_setprio 0
	s_mov_b32 m0, s38
	v_lshl_add_u64 v[222:223], v[242:243], 0, s[8:9]
	s_barrier
	global_load_lds_dwordx4 v[222:223], off
	v_lshl_add_u64 v[222:223], v[244:245], 0, s[8:9]
	s_mov_b32 m0, s39
	s_nop 0
	global_load_lds_dwordx4 v[222:223], off
	s_barrier
	s_waitcnt lgkmcnt(0)
	s_setprio 1
	s_waitcnt lgkmcnt(0)
	v_mfma_scale_f32_16x16x128_f8f6f4 v[110:113], v[2:9], v[18:25], v[110:113], v209, v208 op_sel_hi:[0,0,0]
	v_mfma_scale_f32_16x16x128_f8f6f4 v[106:109], v[10:17], v[18:25], v[106:109], v209, v208 op_sel_hi:[0,0,0]
	v_mfma_scale_f32_16x16x128_f8f6f4 v[102:105], v[2:9], v[26:33], v[102:105], v209, v208 op_sel_hi:[0,0,0]
	v_mfma_scale_f32_16x16x128_f8f6f4 v[98:101], v[10:17], v[26:33], v[98:101], v209, v208 op_sel_hi:[0,0,0]
	v_mfma_scale_f32_16x16x128_f8f6f4 v[78:81], v[2:9], v[34:41], v[78:81], v209, v208 op_sel_hi:[0,0,0]
	v_mfma_scale_f32_16x16x128_f8f6f4 v[74:77], v[10:17], v[34:41], v[74:77], v209, v208 op_sel_hi:[0,0,0]
	v_mfma_scale_f32_16x16x128_f8f6f4 v[70:73], v[2:9], v[42:49], v[70:73], v209, v208 op_sel_hi:[0,0,0]
	v_mfma_scale_f32_16x16x128_f8f6f4 v[66:69], v[10:17], v[42:49], v[66:69], v209, v208 op_sel_hi:[0,0,0]
	s_setprio 0
	s_barrier
	s_add_u32 s22, s22, 0x10080
	s_addc_u32 s23, s23, 0
	s_mov_b32 m0, s54
	v_lshl_add_u64 v[2:3], s[22:23], 0, v[188:189]
	global_load_lds_dwordx4 v[2:3], off
	v_lshl_add_u64 v[2:3], s[22:23], 0, v[186:187]
	s_add_i32 m0, s54, 0x2000
	s_nop 0
	global_load_lds_dwordx4 v[2:3], off
	s_waitcnt vmcnt(6)
	s_barrier
	s_setprio 1
	v_mfma_scale_f32_16x16x128_f8f6f4 v[94:97], v[50:57], v[18:25], v[94:97], v209, v208 op_sel_hi:[0,0,0]
	v_mfma_scale_f32_16x16x128_f8f6f4 v[90:93], v[214:221], v[18:25], v[90:93], v209, v208 op_sel_hi:[0,0,0]
	v_mfma_scale_f32_16x16x128_f8f6f4 v[86:89], v[50:57], v[26:33], v[86:89], v209, v208 op_sel_hi:[0,0,0]
	v_mfma_scale_f32_16x16x128_f8f6f4 v[82:85], v[214:221], v[26:33], v[82:85], v209, v208 op_sel_hi:[0,0,0]
	v_mfma_scale_f32_16x16x128_f8f6f4 v[62:65], v[50:57], v[34:41], v[62:65], v209, v208 op_sel_hi:[0,0,0]
	v_mfma_scale_f32_16x16x128_f8f6f4 v[58:61], v[214:221], v[34:41], v[58:61], v209, v208 op_sel_hi:[0,0,0]
	v_mfma_scale_f32_16x16x128_f8f6f4 v[54:57], v[50:57], v[42:49], v[230:233], v209, v208 op_sel_hi:[0,0,0]
	v_mfma_scale_f32_16x16x128_f8f6f4 v[50:53], v[214:221], v[42:49], v[234:237], v209, v208 op_sel_hi:[0,0,0]
	s_setprio 0
	s_cmp_ge_i32 s59, s1
	s_barrier
	s_cbranch_scc1 .LBB0_1668
	s_mov_b64 s[22:23], s[24:25]
	s_branch .LBB0_1673

.LBB0_1675:
	s_add_i32 s59, s59, 2
	s_add_u32 s24, s22, 0x100
	s_addc_u32 s25, s23, 0
	s_and_b64 s[28:29], s[26:27], exec
	s_cselect_b32 s28, 0, s24
	s_cselect_b32 s29, 0, s25
	s_add_u32 s28, s12, s28
	s_addc_u32 s29, s13, s29
	s_add_u32 s60, s57, s22
	s_addc_u32 s61, s58, s23
	s_and_b64 s[22:23], s[26:27], exec
	s_cselect_b32 s23, s55, s61
	s_cselect_b32 s22, s56, s60
	s_mov_b32 m0, s5
	s_waitcnt lgkmcnt(0)
	v_mfma_scale_f32_16x16x128_f8f6f4 v[222:225], v[2:9], v[42:49], v[142:145], v209, v208 op_sel_hi:[0,0,0]
	v_lshl_add_u64 v[238:239], s[22:23], 0, v[188:189]
	v_add_u32_e32 v191, s46, v203
	v_lshl_add_u64 v[240:241], s[22:23], 0, v[186:187]
	v_mov_b32_e32 v193, v185
	v_mov_b32_e32 v195, v185
	s_nop 1
	v_add_u32_e32 v142, s46, v202
	v_mfma_scale_f32_16x16x128_f8f6f4 v[226:229], v[10:17], v[42:49], v[138:141], v209, v208 op_sel_hi:[0,0,0]
	s_nop 6
	ds_read_b128 v[138:141], v142
	ds_read_b128 v[214:217], v142 offset:2048
	ds_read_b128 v[142:145], v191
	ds_read_b128 v[218:221], v191 offset:2048
	global_load_lds_dwordx4 v[238:239], off
	s_mov_b32 m0, s31
	s_nop 0
	global_load_lds_dwordx4 v[240:241], off
	v_mfma_scale_f32_16x16x128_f8f6f4 v[174:177], v[2:9], v[26:33], v[174:177], v209, v208 op_sel_hi:[0,0,0]
	s_barrier
	s_waitcnt lgkmcnt(0)
	v_mfma_scale_f32_16x16x128_f8f6f4 v[170:173], v[10:17], v[26:33], v[170:173], v209, v208 op_sel_hi:[0,0,0]
	v_mfma_scale_f32_16x16x128_f8f6f4 v[166:169], v[2:9], v[18:25], v[166:169], v209, v208 op_sel_hi:[0,0,0]
	v_mfma_scale_f32_16x16x128_f8f6f4 v[162:165], v[10:17], v[18:25], v[162:165], v209, v208 op_sel_hi:[0,0,0]
	v_mfma_scale_f32_16x16x128_f8f6f4 v[134:137], v[2:9], v[34:41], v[134:137], v209, v208 op_sel_hi:[0,0,0]
	v_mfma_scale_f32_16x16x128_f8f6f4 v[122:125], v[10:17], v[34:41], v[122:125], v209, v208 op_sel_hi:[0,0,0]
	s_setprio 1
	s_waitcnt lgkmcnt(0)
	v_mfma_scale_f32_16x16x128_f8f6f4 v[158:161], v[138:145], v[26:33], v[158:161], v209, v208 op_sel_hi:[0,0,0]
	v_mfma_scale_f32_16x16x128_f8f6f4 v[154:157], v[214:221], v[26:33], v[154:157], v209, v208 op_sel_hi:[0,0,0]
	ds_read_b128 v[26:29], v206 offset:18432
	ds_read_b128 v[30:33], v207 offset:18432
	v_mfma_scale_f32_16x16x128_f8f6f4 v[150:153], v[138:145], v[18:25], v[150:153], v209, v208 op_sel_hi:[0,0,0]
	v_mfma_scale_f32_16x16x128_f8f6f4 v[146:149], v[214:221], v[18:25], v[146:149], v209, v208 op_sel_hi:[0,0,0]
	ds_read_b128 v[18:21], v206 offset:16384
	ds_read_b128 v[22:25], v207 offset:16384
	v_mfma_scale_f32_16x16x128_f8f6f4 v[130:133], v[138:145], v[42:49], v[130:133], v209, v208 op_sel_hi:[0,0,0]
	v_mfma_scale_f32_16x16x128_f8f6f4 v[126:129], v[214:221], v[42:49], v[126:129], v209, v208 op_sel_hi:[0,0,0]
	ds_read_b128 v[42:45], v206 offset:22528
	ds_read_b128 v[46:49], v207 offset:22528
	v_mfma_scale_f32_16x16x128_f8f6f4 v[118:121], v[138:145], v[34:41], v[118:121], v209, v208 op_sel_hi:[0,0,0]
	v_mfma_scale_f32_16x16x128_f8f6f4 v[114:117], v[214:221], v[34:41], v[114:117], v209, v208 op_sel_hi:[0,0,0]
	ds_read_b128 v[34:37], v206 offset:20480
	ds_read_b128 v[38:41], v207 offset:20480
	s_setprio 0
	s_mov_b32 m0, s4
	s_barrier
	global_load_lds_dwordx4 v184, s[28:29]
	s_mov_b32 m0, s33
	v_mov_b32_e32 v191, v185
	global_load_lds_dwordx4 v190, s[28:29]
	s_barrier
	s_waitcnt lgkmcnt(0)
	v_lshl_add_u64 v[242:243], s[28:29], 0, v[184:185]
	v_lshl_add_u64 v[244:245], s[28:29], 0, v[190:191]
	s_setprio 1
	s_waitcnt lgkmcnt(0)
	v_mfma_scale_f32_16x16x128_f8f6f4 v[110:113], v[2:9], v[18:25], v[110:113], v209, v208 op_sel_hi:[0,0,0]
	v_mfma_scale_f32_16x16x128_f8f6f4 v[106:109], v[10:17], v[18:25], v[106:109], v209, v208 op_sel_hi:[0,0,0]
	v_mfma_scale_f32_16x16x128_f8f6f4 v[102:105], v[2:9], v[26:33], v[102:105], v209, v208 op_sel_hi:[0,0,0]
	v_mfma_scale_f32_16x16x128_f8f6f4 v[98:101], v[10:17], v[26:33], v[98:101], v209, v208 op_sel_hi:[0,0,0]
	v_mfma_scale_f32_16x16x128_f8f6f4 v[78:81], v[2:9], v[34:41], v[78:81], v209, v208 op_sel_hi:[0,0,0]
	v_mfma_scale_f32_16x16x128_f8f6f4 v[74:77], v[10:17], v[34:41], v[74:77], v209, v208 op_sel_hi:[0,0,0]
	v_mfma_scale_f32_16x16x128_f8f6f4 v[70:73], v[2:9], v[42:49], v[70:73], v209, v208 op_sel_hi:[0,0,0]
	v_mfma_scale_f32_16x16x128_f8f6f4 v[66:69], v[10:17], v[42:49], v[66:69], v209, v208 op_sel_hi:[0,0,0]
	s_setprio 0
	s_barrier
	s_add_u32 s26, s22, 0x10000
	s_addc_u32 s27, s23, 0
	s_mov_b32 m0, s48
	v_lshl_add_u64 v[2:3], s[26:27], 0, v[188:189]
	global_load_lds_dwordx4 v[2:3], off
	v_lshl_add_u64 v[2:3], s[26:27], 0, v[186:187]
	s_mov_b32 m0, s49
	s_nop 0
	global_load_lds_dwordx4 v[2:3], off
	s_waitcnt vmcnt(6)
	s_barrier
	s_setprio 1
	v_mfma_scale_f32_16x16x128_f8f6f4 v[94:97], v[138:145], v[18:25], v[94:97], v209, v208 op_sel_hi:[0,0,0]
	v_mfma_scale_f32_16x16x128_f8f6f4 v[90:93], v[214:221], v[18:25], v[90:93], v209, v208 op_sel_hi:[0,0,0]
	ds_read_b128 v[18:21], v206 offset:32768
	ds_read_b128 v[22:25], v207 offset:32768
	v_mfma_scale_f32_16x16x128_f8f6f4 v[86:89], v[138:145], v[26:33], v[86:89], v209, v208 op_sel_hi:[0,0,0]
	v_mfma_scale_f32_16x16x128_f8f6f4 v[82:85], v[214:221], v[26:33], v[82:85], v209, v208 op_sel_hi:[0,0,0]
	ds_read_b128 v[26:29], v206 offset:34816
	ds_read_b128 v[30:33], v207 offset:34816
	v_mfma_scale_f32_16x16x128_f8f6f4 v[62:65], v[138:145], v[34:41], v[62:65], v209, v208 op_sel_hi:[0,0,0]
	v_mfma_scale_f32_16x16x128_f8f6f4 v[58:61], v[214:221], v[34:41], v[58:61], v209, v208 op_sel_hi:[0,0,0]
	ds_read_b128 v[34:37], v206 offset:36864
	ds_read_b128 v[38:41], v207 offset:36864
	v_mfma_scale_f32_16x16x128_f8f6f4 v[230:233], v[138:145], v[42:49], v[54:57], v209, v208 op_sel_hi:[0,0,0]
	v_mfma_scale_f32_16x16x128_f8f6f4 v[234:237], v[214:221], v[42:49], v[50:53], v209, v208 op_sel_hi:[0,0,0]
	ds_read_b128 v[42:45], v206 offset:38912
	ds_read_b128 v[46:49], v207 offset:38912
	s_setprio 0
	v_add_u32_e32 v6, s50, v202
	v_add_u32_e32 v14, s50, v203
	s_barrier
	ds_read_b128 v[2:5], v6
	ds_read_b128 v[10:13], v6 offset:2048
	ds_read_b128 v[6:9], v14
	ds_read_b128 v[14:17], v14 offset:2048
	s_mov_b32 m0, s34
	v_lshl_add_u64 v[50:51], s[28:29], 0, v[192:193]
	global_load_lds_dwordx4 v[50:51], off
	v_lshl_add_u64 v[50:51], s[28:29], 0, v[194:195]
	s_mov_b32 m0, s35
	s_nop 0
	global_load_lds_dwordx4 v[50:51], off
	s_waitcnt lgkmcnt(8)
	s_barrier
	s_waitcnt lgkmcnt(0)
	s_setprio 1
	s_waitcnt lgkmcnt(0)
	v_mfma_scale_f32_16x16x128_f8f6f4 v[174:177], v[2:9], v[18:25], v[174:177], v209, v208 op_sel_hi:[0,0,0]
	v_mfma_scale_f32_16x16x128_f8f6f4 v[170:173], v[10:17], v[18:25], v[170:173], v209, v208 op_sel_hi:[0,0,0]
	v_mfma_scale_f32_16x16x128_f8f6f4 v[166:169], v[2:9], v[26:33], v[166:169], v209, v208 op_sel_hi:[0,0,0]
	v_mfma_scale_f32_16x16x128_f8f6f4 v[162:165], v[10:17], v[26:33], v[162:165], v209, v208 op_sel_hi:[0,0,0]
	v_mfma_scale_f32_16x16x128_f8f6f4 v[142:145], v[2:9], v[34:41], v[222:225], v209, v208 op_sel_hi:[0,0,0]
	v_mfma_scale_f32_16x16x128_f8f6f4 v[138:141], v[10:17], v[34:41], v[226:229], v209, v208 op_sel_hi:[0,0,0]
	v_mfma_scale_f32_16x16x128_f8f6f4 v[134:137], v[2:9], v[42:49], v[134:137], v209, v208 op_sel_hi:[0,0,0]
	v_mfma_scale_f32_16x16x128_f8f6f4 v[122:125], v[10:17], v[42:49], v[122:125], v209, v208 op_sel_hi:[0,0,0]
	s_setprio 0
	s_barrier
	s_mov_b32 m0, s52
	v_add_u32_e32 v54, s51, v202
	v_lshl_add_u64 v[222:223], v[238:239], 0, s[8:9]
	v_add_u32_e32 v191, s51, v203
	ds_read_b128 v[50:53], v54
	ds_read_b128 v[214:217], v54 offset:2048
	ds_read_b128 v[54:57], v191
	ds_read_b128 v[218:221], v191 offset:2048
	global_load_lds_dwordx4 v[222:223], off
	v_lshl_add_u64 v[222:223], v[240:241], 0, s[8:9]
	s_mov_b32 m0, s53
	s_nop 0
	global_load_lds_dwordx4 v[222:223], off
	s_barrier
	s_waitcnt lgkmcnt(0)
	s_setprio 1
	s_waitcnt lgkmcnt(0)
	v_mfma_scale_f32_16x16x128_f8f6f4 v[158:161], v[50:57], v[18:25], v[158:161], v209, v208 op_sel_hi:[0,0,0]
	v_mfma_scale_f32_16x16x128_f8f6f4 v[154:157], v[214:221], v[18:25], v[154:157], v209, v208 op_sel_hi:[0,0,0]
	ds_read_b128 v[18:21], v206 offset:49152
	ds_read_b128 v[22:25], v207 offset:49152
	v_mfma_scale_f32_16x16x128_f8f6f4 v[150:153], v[50:57], v[26:33], v[150:153], v209, v208 op_sel_hi:[0,0,0]
	v_mfma_scale_f32_16x16x128_f8f6f4 v[146:149], v[214:221], v[26:33], v[146:149], v209, v208 op_sel_hi:[0,0,0]
	ds_read_b128 v[26:29], v206 offset:51200
	ds_read_b128 v[30:33], v207 offset:51200
	v_mfma_scale_f32_16x16x128_f8f6f4 v[130:133], v[50:57], v[34:41], v[130:133], v209, v208 op_sel_hi:[0,0,0]
	v_mfma_scale_f32_16x16x128_f8f6f4 v[126:129], v[214:221], v[34:41], v[126:129], v209, v208 op_sel_hi:[0,0,0]
	ds_read_b128 v[34:37], v206 offset:53248
	ds_read_b128 v[38:41], v207 offset:53248
	v_mfma_scale_f32_16x16x128_f8f6f4 v[118:121], v[50:57], v[42:49], v[118:121], v209, v208 op_sel_hi:[0,0,0]
	v_mfma_scale_f32_16x16x128_f8f6f4 v[114:117], v[214:221], v[42:49], v[114:117], v209, v208 op_sel_hi:[0,0,0]
	ds_read_b128 v[42:45], v206 offset:55296
	ds_read_b128 v[46:49], v207 offset:55296
	s_setprio 0
	s_mov_b32 m0, s38
	v_lshl_add_u64 v[222:223], v[242:243], 0, s[8:9]
	s_barrier
	global_load_lds_dwordx4 v[222:223], off
	v_lshl_add_u64 v[222:223], v[244:245], 0, s[8:9]
	s_mov_b32 m0, s39
	s_nop 0
	global_load_lds_dwordx4 v[222:223], off
	s_barrier
	s_waitcnt lgkmcnt(0)
	s_setprio 1
	s_waitcnt lgkmcnt(0)
	v_mfma_scale_f32_16x16x128_f8f6f4 v[110:113], v[2:9], v[18:25], v[110:113], v209, v208 op_sel_hi:[0,0,0]
	v_mfma_scale_f32_16x16x128_f8f6f4 v[106:109], v[10:17], v[18:25], v[106:109], v209, v208 op_sel_hi:[0,0,0]
	v_mfma_scale_f32_16x16x128_f8f6f4 v[102:105], v[2:9], v[26:33], v[102:105], v209, v208 op_sel_hi:[0,0,0]
	v_mfma_scale_f32_16x16x128_f8f6f4 v[98:101], v[10:17], v[26:33], v[98:101], v209, v208 op_sel_hi:[0,0,0]
	v_mfma_scale_f32_16x16x128_f8f6f4 v[78:81], v[2:9], v[34:41], v[78:81], v209, v208 op_sel_hi:[0,0,0]
	v_mfma_scale_f32_16x16x128_f8f6f4 v[74:77], v[10:17], v[34:41], v[74:77], v209, v208 op_sel_hi:[0,0,0]
	v_mfma_scale_f32_16x16x128_f8f6f4 v[70:73], v[2:9], v[42:49], v[70:73], v209, v208 op_sel_hi:[0,0,0]
	v_mfma_scale_f32_16x16x128_f8f6f4 v[66:69], v[10:17], v[42:49], v[66:69], v209, v208 op_sel_hi:[0,0,0]
	s_setprio 0
	s_barrier
	s_add_u32 s22, s22, 0x10080
	s_addc_u32 s23, s23, 0
	s_mov_b32 m0, s54
	v_lshl_add_u64 v[2:3], s[22:23], 0, v[188:189]
	global_load_lds_dwordx4 v[2:3], off
	v_lshl_add_u64 v[2:3], s[22:23], 0, v[186:187]
	s_add_i32 m0, s54, 0x2000
	s_nop 0
	global_load_lds_dwordx4 v[2:3], off
	s_waitcnt vmcnt(6)
	s_barrier
	s_setprio 1
	v_mfma_scale_f32_16x16x128_f8f6f4 v[94:97], v[50:57], v[18:25], v[94:97], v209, v208 op_sel_hi:[0,0,0]
	v_mfma_scale_f32_16x16x128_f8f6f4 v[90:93], v[214:221], v[18:25], v[90:93], v209, v208 op_sel_hi:[0,0,0]
	v_mfma_scale_f32_16x16x128_f8f6f4 v[86:89], v[50:57], v[26:33], v[86:89], v209, v208 op_sel_hi:[0,0,0]
	v_mfma_scale_f32_16x16x128_f8f6f4 v[82:85], v[214:221], v[26:33], v[82:85], v209, v208 op_sel_hi:[0,0,0]
	v_mfma_scale_f32_16x16x128_f8f6f4 v[62:65], v[50:57], v[34:41], v[62:65], v209, v208 op_sel_hi:[0,0,0]
	v_mfma_scale_f32_16x16x128_f8f6f4 v[58:61], v[214:221], v[34:41], v[58:61], v209, v208 op_sel_hi:[0,0,0]
	v_mfma_scale_f32_16x16x128_f8f6f4 v[54:57], v[50:57], v[42:49], v[230:233], v209, v208 op_sel_hi:[0,0,0]
	v_mfma_scale_f32_16x16x128_f8f6f4 v[50:53], v[214:221], v[42:49], v[234:237], v209, v208 op_sel_hi:[0,0,0]
	s_setprio 0
	s_cmp_ge_i32 s59, s1
	s_barrier
	s_cbranch_scc1 .LBB0_1668
	s_mov_b64 s[22:23], s[24:25]
	s_branch .LBB0_1673
